# MoE down GEMM: no pipeline drain before the K-loop (epilogue loads are waited where issued); LN1/router: no barrier after the top-4 step
# speedup vs baseline: 1.0335x; 1.0038x over previous
; template <bool SKIP_MIX>
; __device__ __forceinline__ void p8_ln_router(Frame& F0, const In& I) {
;     ...
;         }
;         __syncthreads();
;     }
.LBB0_1513:
	s_or_b64 exec, exec, s[0:1]
	s_add_i32 s22, s22, s84
	s_cmpk_gt_i32 s22, 0x7ff
	s_waitcnt lgkmcnt(0)
	s_cbranch_scc1 .LBB0_1518

; #define LAS __attribute__((address_space(3)))
; template <bool SKIP_MIX>
; __device__ __forceinline__ void p8_ln_router(Frame& F0, const In& I) {
;     ...
;         const LAS float* ap = hs + col * P8_PITCH + 256 * w + 4 * kq;
;         const float* bp = I.w_router + (size_t)(256 * w + 4 * kq) * NE + col;
; #pragma unroll 4
;         for (int kk = 0; kk < 16; ++kk) {
;             const f32x4 a = *(const LAS f32x4*)(ap + 16 * kk);
; #pragma unroll
;             for (int e = 0; e < 4; ++e) {
;                 const float b0 = bp[(size_t)(16 * kk + e) * NE], b1 = bp[(size_t)(16 * kk + e) * NE + 16];
;                 c0 = __builtin_amdgcn_mfma_f32_16x16x4f32(a[e], b0, c0, 0, 0, 0);
;                 c1 = __builtin_amdgcn_mfma_f32_16x16x4f32(a[e], b1, c1, 0, 0, 0);
;             }
;         }
.LBB0_1515:
	s_waitcnt vmcnt(19)
	s_mov_b64 s[0:1], 0x1000
	v_mov_b32_e32 v108, v88
	v_mov_b32_e32 v109, v89
	global_load_dword v117, v[108:109], off offset:0
	global_load_dword v118, v[108:109], off offset:64
	global_load_dword v119, v[108:109], off offset:128
	global_load_dword v120, v[108:109], off offset:192
	global_load_dword v121, v[108:109], off offset:256
	global_load_dword v122, v[108:109], off offset:320
	global_load_dword v123, v[108:109], off offset:384
	global_load_dword v124, v[108:109], off offset:448
	global_load_dword v125, v[108:109], off offset:2048
	global_load_dword v126, v[108:109], off offset:2112
	global_load_dword v127, v[108:109], off offset:2176
	global_load_dword v128, v[108:109], off offset:2240
	global_load_dword v129, v[108:109], off offset:2304
	global_load_dword v130, v[108:109], off offset:2368
	global_load_dword v131, v[108:109], off offset:2432
	global_load_dword v132, v[108:109], off offset:2496
	v_lshl_add_u64 v[108:109], v[108:109], 0, s[0:1]
	global_load_dword v133, v[108:109], off offset:0
	global_load_dword v134, v[108:109], off offset:64
	global_load_dword v135, v[108:109], off offset:128
	global_load_dword v136, v[108:109], off offset:192
	global_load_dword v137, v[108:109], off offset:256
	global_load_dword v138, v[108:109], off offset:320
	global_load_dword v139, v[108:109], off offset:384
	global_load_dword v140, v[108:109], off offset:448
	global_load_dword v141, v[108:109], off offset:2048
	global_load_dword v142, v[108:109], off offset:2112
	global_load_dword v143, v[108:109], off offset:2176
	global_load_dword v144, v[108:109], off offset:2240
	global_load_dword v145, v[108:109], off offset:2304
	global_load_dword v146, v[108:109], off offset:2368
	global_load_dword v147, v[108:109], off offset:2432
	global_load_dword v148, v[108:109], off offset:2496
	v_lshl_add_u64 v[108:109], v[108:109], 0, s[0:1]
	global_load_dword v149, v[108:109], off offset:0
	global_load_dword v150, v[108:109], off offset:64
	global_load_dword v151, v[108:109], off offset:128
	global_load_dword v160, v[108:109], off offset:192
	global_load_dword v161, v[108:109], off offset:256
	global_load_dword v162, v[108:109], off offset:320
	global_load_dword v163, v[108:109], off offset:384
	global_load_dword v164, v[108:109], off offset:448
	global_load_dword v165, v[108:109], off offset:2048
	global_load_dword v166, v[108:109], off offset:2112
	global_load_dword v167, v[108:109], off offset:2176
	global_load_dword v168, v[108:109], off offset:2240
	ds_read_b128 v[92:95], v90
	ds_read_b128 v[96:99], v90 offset:64
	ds_read_b128 v[100:103], v90 offset:128
	ds_read_b128 v[104:107], v90 offset:192
	s_waitcnt lgkmcnt(3)
	global_load_dword v169, v[108:109], off offset:2304
	s_waitcnt vmcnt(43)
	v_mfma_f32_16x16x4_f32 v[66:69], v92, v117, v[66:69]
	v_mfma_f32_16x16x4_f32 v[70:73], v92, v118, v[70:73]
	global_load_dword v170, v[108:109], off offset:2368
	s_waitcnt vmcnt(42)
	v_mfma_f32_16x16x4_f32 v[66:69], v93, v119, v[66:69]
	v_mfma_f32_16x16x4_f32 v[70:73], v93, v120, v[70:73]
	global_load_dword v171, v[108:109], off offset:2432
	s_waitcnt vmcnt(41)
	v_mfma_f32_16x16x4_f32 v[66:69], v94, v121, v[66:69]
	v_mfma_f32_16x16x4_f32 v[70:73], v94, v122, v[70:73]
	global_load_dword v172, v[108:109], off offset:2496
	s_waitcnt vmcnt(40)
	v_mfma_f32_16x16x4_f32 v[66:69], v95, v123, v[66:69]
	v_mfma_f32_16x16x4_f32 v[70:73], v95, v124, v[70:73]
	s_waitcnt lgkmcnt(2)
	v_lshl_add_u64 v[108:109], v[108:109], 0, s[0:1]
	global_load_dword v173, v[108:109], off offset:0
	s_waitcnt vmcnt(39)
	v_mfma_f32_16x16x4_f32 v[66:69], v96, v125, v[66:69]
	v_mfma_f32_16x16x4_f32 v[70:73], v96, v126, v[70:73]
	global_load_dword v174, v[108:109], off offset:64
	s_waitcnt vmcnt(38)
	v_mfma_f32_16x16x4_f32 v[66:69], v97, v127, v[66:69]
	v_mfma_f32_16x16x4_f32 v[70:73], v97, v128, v[70:73]
	global_load_dword v175, v[108:109], off offset:128
	s_waitcnt vmcnt(37)
	v_mfma_f32_16x16x4_f32 v[66:69], v98, v129, v[66:69]
	v_mfma_f32_16x16x4_f32 v[70:73], v98, v130, v[70:73]
	global_load_dword v176, v[108:109], off offset:192
	s_waitcnt vmcnt(36)
	v_mfma_f32_16x16x4_f32 v[66:69], v99, v131, v[66:69]
	v_mfma_f32_16x16x4_f32 v[70:73], v99, v132, v[70:73]
	s_waitcnt lgkmcnt(1)
	global_load_dword v177, v[108:109], off offset:256
	s_waitcnt vmcnt(35)
	v_mfma_f32_16x16x4_f32 v[66:69], v100, v133, v[66:69]
	v_mfma_f32_16x16x4_f32 v[70:73], v100, v134, v[70:73]
	global_load_dword v178, v[108:109], off offset:320
	s_waitcnt vmcnt(34)
	v_mfma_f32_16x16x4_f32 v[66:69], v101, v135, v[66:69]
	v_mfma_f32_16x16x4_f32 v[70:73], v101, v136, v[70:73]
	global_load_dword v179, v[108:109], off offset:384
	s_waitcnt vmcnt(33)
	v_mfma_f32_16x16x4_f32 v[66:69], v102, v137, v[66:69]
	v_mfma_f32_16x16x4_f32 v[70:73], v102, v138, v[70:73]
	global_load_dword v180, v[108:109], off offset:448
	s_waitcnt vmcnt(32)
	v_mfma_f32_16x16x4_f32 v[66:69], v103, v139, v[66:69]
	v_mfma_f32_16x16x4_f32 v[70:73], v103, v140, v[70:73]
	s_waitcnt lgkmcnt(0)
	global_load_dword v181, v[108:109], off offset:2048
	s_waitcnt vmcnt(31)
	v_mfma_f32_16x16x4_f32 v[66:69], v104, v141, v[66:69]
	v_mfma_f32_16x16x4_f32 v[70:73], v104, v142, v[70:73]
	global_load_dword v182, v[108:109], off offset:2112
	s_waitcnt vmcnt(30)
	v_mfma_f32_16x16x4_f32 v[66:69], v105, v143, v[66:69]
	v_mfma_f32_16x16x4_f32 v[70:73], v105, v144, v[70:73]
	global_load_dword v183, v[108:109], off offset:2176
	s_waitcnt vmcnt(29)
	v_mfma_f32_16x16x4_f32 v[66:69], v106, v145, v[66:69]
	v_mfma_f32_16x16x4_f32 v[70:73], v106, v146, v[70:73]
	global_load_dword v184, v[108:109], off offset:2240
	s_waitcnt vmcnt(28)
; #define LAS __attribute__((address_space(3)))
; template <bool SKIP_MIX>
; __device__ __forceinline__ void p8_ln_router(Frame& F0, const In& I) {
;     ...
;         const LAS float* ap = hs + col * P8_PITCH + 256 * w + 4 * kq;
;         const float* bp = I.w_router + (size_t)(256 * w + 4 * kq) * NE + col;
; #pragma unroll 4
;         for (int kk = 0; kk < 16; ++kk) {
;             const f32x4 a = *(const LAS f32x4*)(ap + 16 * kk);
; #pragma unroll
;             for (int e = 0; e < 4; ++e) {
;                 const float b0 = bp[(size_t)(16 * kk + e) * NE], b1 = bp[(size_t)(16 * kk + e) * NE + 16];
;                 c0 = __builtin_amdgcn_mfma_f32_16x16x4f32(a[e], b0, c0, 0, 0, 0);
;                 c1 = __builtin_amdgcn_mfma_f32_16x16x4f32(a[e], b1, c1, 0, 0, 0);
;             }
;         }
	v_mfma_f32_16x16x4_f32 v[66:69], v107, v147, v[66:69]
	v_mfma_f32_16x16x4_f32 v[70:73], v107, v148, v[70:73]
	ds_read_b128 v[92:95], v90 offset:256
	ds_read_b128 v[96:99], v90 offset:320
	ds_read_b128 v[100:103], v90 offset:384
	ds_read_b128 v[104:107], v90 offset:448
	s_waitcnt lgkmcnt(3)
	global_load_dword v185, v[108:109], off offset:2304
	s_waitcnt vmcnt(27)
	v_mfma_f32_16x16x4_f32 v[66:69], v92, v149, v[66:69]
	v_mfma_f32_16x16x4_f32 v[70:73], v92, v150, v[70:73]
	global_load_dword v186, v[108:109], off offset:2368
	s_waitcnt vmcnt(26)
	v_mfma_f32_16x16x4_f32 v[66:69], v93, v151, v[66:69]
	v_mfma_f32_16x16x4_f32 v[70:73], v93, v160, v[70:73]
	global_load_dword v187, v[108:109], off offset:2432
	s_waitcnt vmcnt(25)
	v_mfma_f32_16x16x4_f32 v[66:69], v94, v161, v[66:69]
	v_mfma_f32_16x16x4_f32 v[70:73], v94, v162, v[70:73]
	global_load_dword v188, v[108:109], off offset:2496
	s_waitcnt vmcnt(24)
	v_mfma_f32_16x16x4_f32 v[66:69], v95, v163, v[66:69]
	v_mfma_f32_16x16x4_f32 v[70:73], v95, v164, v[70:73]
	s_waitcnt lgkmcnt(2)
	v_lshl_add_u64 v[108:109], v[108:109], 0, s[0:1]
	global_load_dword v189, v[108:109], off offset:0
	s_waitcnt vmcnt(23)
	v_mfma_f32_16x16x4_f32 v[66:69], v96, v165, v[66:69]
	v_mfma_f32_16x16x4_f32 v[70:73], v96, v166, v[70:73]
	global_load_dword v190, v[108:109], off offset:64
	s_waitcnt vmcnt(22)
	v_mfma_f32_16x16x4_f32 v[66:69], v97, v167, v[66:69]
	v_mfma_f32_16x16x4_f32 v[70:73], v97, v168, v[70:73]
	global_load_dword v191, v[108:109], off offset:128
	s_waitcnt vmcnt(21)
	v_mfma_f32_16x16x4_f32 v[66:69], v98, v169, v[66:69]
	v_mfma_f32_16x16x4_f32 v[70:73], v98, v170, v[70:73]
	global_load_dword v192, v[108:109], off offset:192
	s_waitcnt vmcnt(20)
	v_mfma_f32_16x16x4_f32 v[66:69], v99, v171, v[66:69]
	v_mfma_f32_16x16x4_f32 v[70:73], v99, v172, v[70:73]
	s_waitcnt lgkmcnt(1)
	global_load_dword v193, v[108:109], off offset:256
	s_waitcnt vmcnt(19)
	v_mfma_f32_16x16x4_f32 v[66:69], v100, v173, v[66:69]
	v_mfma_f32_16x16x4_f32 v[70:73], v100, v174, v[70:73]
	global_load_dword v194, v[108:109], off offset:320
	s_waitcnt vmcnt(18)
	v_mfma_f32_16x16x4_f32 v[66:69], v101, v175, v[66:69]
	v_mfma_f32_16x16x4_f32 v[70:73], v101, v176, v[70:73]
	global_load_dword v195, v[108:109], off offset:384
	s_waitcnt vmcnt(17)
	v_mfma_f32_16x16x4_f32 v[66:69], v102, v177, v[66:69]
	v_mfma_f32_16x16x4_f32 v[70:73], v102, v178, v[70:73]
	global_load_dword v196, v[108:109], off offset:448
	s_waitcnt vmcnt(16)
	v_mfma_f32_16x16x4_f32 v[66:69], v103, v179, v[66:69]
	v_mfma_f32_16x16x4_f32 v[70:73], v103, v180, v[70:73]
	s_waitcnt lgkmcnt(0)
	global_load_dword v197, v[108:109], off offset:2048
	s_waitcnt vmcnt(15)
	v_mfma_f32_16x16x4_f32 v[66:69], v104, v181, v[66:69]
	v_mfma_f32_16x16x4_f32 v[70:73], v104, v182, v[70:73]
	global_load_dword v198, v[108:109], off offset:2112
	s_waitcnt vmcnt(14)
	v_mfma_f32_16x16x4_f32 v[66:69], v105, v183, v[66:69]
	v_mfma_f32_16x16x4_f32 v[70:73], v105, v184, v[70:73]
	global_load_dword v199, v[108:109], off offset:2176
	s_waitcnt vmcnt(13)
	v_mfma_f32_16x16x4_f32 v[66:69], v106, v185, v[66:69]
	v_mfma_f32_16x16x4_f32 v[70:73], v106, v186, v[70:73]
	s_waitcnt vmcnt(11)
	v_mfma_f32_16x16x4_f32 v[66:69], v107, v187, v[66:69]
	v_mfma_f32_16x16x4_f32 v[70:73], v107, v188, v[70:73]
	ds_read_b128 v[92:95], v90 offset:512
	ds_read_b128 v[96:99], v90 offset:576
	ds_read_b128 v[100:103], v90 offset:640
	ds_read_b128 v[104:107], v90 offset:704
	s_waitcnt lgkmcnt(3)
	s_waitcnt vmcnt(9)
	v_mfma_f32_16x16x4_f32 v[66:69], v92, v189, v[66:69]
	v_mfma_f32_16x16x4_f32 v[70:73], v92, v190, v[70:73]
	s_waitcnt vmcnt(7)
	v_mfma_f32_16x16x4_f32 v[66:69], v93, v191, v[66:69]
	v_mfma_f32_16x16x4_f32 v[70:73], v93, v192, v[70:73]
	s_waitcnt vmcnt(5)
	v_mfma_f32_16x16x4_f32 v[66:69], v94, v193, v[66:69]
	v_mfma_f32_16x16x4_f32 v[70:73], v94, v194, v[70:73]
	s_waitcnt vmcnt(3)
	v_mfma_f32_16x16x4_f32 v[66:69], v95, v195, v[66:69]
	v_mfma_f32_16x16x4_f32 v[70:73], v95, v196, v[70:73]
	s_waitcnt lgkmcnt(2)
	s_waitcnt vmcnt(1)
	v_mfma_f32_16x16x4_f32 v[66:69], v96, v197, v[66:69]
	v_mfma_f32_16x16x4_f32 v[70:73], v96, v198, v[70:73]
	s_waitcnt vmcnt(0)
	v_mfma_f32_16x16x4_f32 v[66:69], v97, v199, v[66:69]
	v_mfma_f32_16x16x4_f32 v[70:73], v97, v200, v[70:73]
	v_mfma_f32_16x16x4_f32 v[66:69], v98, v201, v[66:69]
	v_mfma_f32_16x16x4_f32 v[70:73], v98, v202, v[70:73]
	v_mfma_f32_16x16x4_f32 v[66:69], v99, v203, v[66:69]
	v_mfma_f32_16x16x4_f32 v[70:73], v99, v204, v[70:73]
	s_waitcnt lgkmcnt(1)
	v_mfma_f32_16x16x4_f32 v[66:69], v100, v205, v[66:69]
	v_mfma_f32_16x16x4_f32 v[70:73], v100, v206, v[70:73]
	v_mfma_f32_16x16x4_f32 v[66:69], v101, v207, v[66:69]
	v_mfma_f32_16x16x4_f32 v[70:73], v101, v208, v[70:73]
	v_mfma_f32_16x16x4_f32 v[66:69], v102, v209, v[66:69]
	v_mfma_f32_16x16x4_f32 v[70:73], v102, v210, v[70:73]
	v_mfma_f32_16x16x4_f32 v[66:69], v103, v211, v[66:69]
	v_mfma_f32_16x16x4_f32 v[70:73], v103, v212, v[70:73]
	s_waitcnt lgkmcnt(0)
	v_mfma_f32_16x16x4_f32 v[66:69], v104, v213, v[66:69]
	v_mfma_f32_16x16x4_f32 v[70:73], v104, v214, v[70:73]
	v_mfma_f32_16x16x4_f32 v[66:69], v105, v215, v[66:69]
	v_mfma_f32_16x16x4_f32 v[70:73], v105, v216, v[70:73]
	v_mfma_f32_16x16x4_f32 v[66:69], v106, v217, v[66:69]
	v_mfma_f32_16x16x4_f32 v[70:73], v106, v218, v[70:73]
	v_mfma_f32_16x16x4_f32 v[66:69], v107, v219, v[66:69]
	v_mfma_f32_16x16x4_f32 v[70:73], v107, v220, v[70:73]
	ds_read_b128 v[92:95], v90 offset:768
	ds_read_b128 v[96:99], v90 offset:832
	ds_read_b128 v[100:103], v90 offset:896
	ds_read_b128 v[104:107], v90 offset:960
	s_waitcnt lgkmcnt(3)
; #define LAS __attribute__((address_space(3)))
; template <bool SKIP_MIX>
; __device__ __forceinline__ void p8_ln_router(Frame& F0, const In& I) {
;     ...
;         for (int kk = 0; kk < 16; ++kk) {
;             const f32x4 a = *(const LAS f32x4*)(ap + 16 * kk);
; #pragma unroll
;             for (int e = 0; e < 4; ++e) {
;                 const float b0 = bp[(size_t)(16 * kk + e) * NE], b1 = bp[(size_t)(16 * kk + e) * NE + 16];
;                 c0 = __builtin_amdgcn_mfma_f32_16x16x4f32(a[e], b0, c0, 0, 0, 0);
;                 c1 = __builtin_amdgcn_mfma_f32_16x16x4f32(a[e], b1, c1, 0, 0, 0);
;             }
;         }
; #pragma unroll
;         for (int i = 0; i < 4; ++i) { part[(w * 16 + 4 * kq + i) * 32 + col] = c0[i]; part[(w * 16 + 4 * kq + i) * 32 + 16 + col] = c1[i]; }
;         __syncthreads();
;         { const int tl = F.tid >> 5, e = F.tid & 31; float s = I.b_router[e];
; #pragma unroll
;             for (int ww = 0; ww < 8; ++ww) s += part[(ww * 16 + tl) * 32 + e];
;             lg[tl * 32 + e] = s; }
;         __syncthreads();
;         if (F.tid < 16) {
;             const int tl = F.tid; float lv[32];
; #pragma unroll
;             for (int e = 0; e < 32; ++e) lv[e] = lg[tl * 32 + e];
;             int ti[4]; float tv[4];
; #pragma unroll
;             for (int k = 0; k < 4; ++k) { float best = -3.4e38f; int bi = 0;
; #pragma unroll
;                 for (int e = 0; e < 32; ++e) { const bool tk = lv[e] > best; best = tk ? lv[e] : best; bi = tk ? e : bi; }
	v_mfma_f32_16x16x4_f32 v[66:69], v92, v221, v[66:69]
	v_mfma_f32_16x16x4_f32 v[70:73], v92, v222, v[70:73]
	v_mfma_f32_16x16x4_f32 v[66:69], v93, v223, v[66:69]
	v_mfma_f32_16x16x4_f32 v[70:73], v93, v224, v[70:73]
	v_mfma_f32_16x16x4_f32 v[66:69], v94, v225, v[66:69]
	v_mfma_f32_16x16x4_f32 v[70:73], v94, v226, v[70:73]
	v_mfma_f32_16x16x4_f32 v[66:69], v95, v227, v[66:69]
	v_mfma_f32_16x16x4_f32 v[70:73], v95, v228, v[70:73]
	s_waitcnt lgkmcnt(2)
	v_mfma_f32_16x16x4_f32 v[66:69], v96, v229, v[66:69]
	v_mfma_f32_16x16x4_f32 v[70:73], v96, v230, v[70:73]
	v_mfma_f32_16x16x4_f32 v[66:69], v97, v231, v[66:69]
	v_mfma_f32_16x16x4_f32 v[70:73], v97, v232, v[70:73]
	v_mfma_f32_16x16x4_f32 v[66:69], v98, v233, v[66:69]
	v_mfma_f32_16x16x4_f32 v[70:73], v98, v234, v[70:73]
	v_mfma_f32_16x16x4_f32 v[66:69], v99, v235, v[66:69]
	v_mfma_f32_16x16x4_f32 v[70:73], v99, v236, v[70:73]
	s_waitcnt lgkmcnt(1)
	v_mfma_f32_16x16x4_f32 v[66:69], v100, v237, v[66:69]
	v_mfma_f32_16x16x4_f32 v[70:73], v100, v238, v[70:73]
	v_mfma_f32_16x16x4_f32 v[66:69], v101, v239, v[66:69]
	v_mfma_f32_16x16x4_f32 v[70:73], v101, v240, v[70:73]
	v_mfma_f32_16x16x4_f32 v[66:69], v102, v241, v[66:69]
	v_mfma_f32_16x16x4_f32 v[70:73], v102, v242, v[70:73]
	v_mfma_f32_16x16x4_f32 v[66:69], v103, v243, v[66:69]
	v_mfma_f32_16x16x4_f32 v[70:73], v103, v244, v[70:73]
	s_waitcnt lgkmcnt(0)
	v_mfma_f32_16x16x4_f32 v[66:69], v104, v245, v[66:69]
	v_mfma_f32_16x16x4_f32 v[70:73], v104, v246, v[70:73]
	v_mfma_f32_16x16x4_f32 v[66:69], v105, v247, v[66:69]
	v_mfma_f32_16x16x4_f32 v[70:73], v105, v248, v[70:73]
	v_mfma_f32_16x16x4_f32 v[66:69], v106, v249, v[66:69]
	v_mfma_f32_16x16x4_f32 v[70:73], v106, v250, v[70:73]
	v_mfma_f32_16x16x4_f32 v[66:69], v107, v251, v[66:69]
	v_mfma_f32_16x16x4_f32 v[70:73], v107, v252, v[70:73]
	s_nop 8
	ds_write2_b32 v156, v66, v70 offset1:16
	ds_write2_b32 v156, v67, v71 offset0:32 offset1:48
	ds_write2_b32 v156, v68, v72 offset0:64 offset1:80
	ds_write2_b32 v156, v69, v73 offset0:96 offset1:112
	s_waitcnt lgkmcnt(0)
	s_barrier
	ds_read2st64_b32 v[66:67], v153 offset1:8
	ds_read2st64_b32 v[68:69], v153 offset0:16 offset1:24
	ds_read2st64_b32 v[70:71], v153 offset0:32 offset1:40
	ds_read2st64_b32 v[72:73], v153 offset0:48 offset1:56
	s_waitcnt lgkmcnt(3)
	v_add_f32_e32 v66, v253, v66
	v_add_f32_e32 v66, v66, v67
	s_waitcnt lgkmcnt(2)
	v_add_f32_e32 v66, v66, v68
	v_add_f32_e32 v66, v66, v69
	s_waitcnt lgkmcnt(1)
	v_add_f32_e32 v66, v66, v70
	v_add_f32_e32 v66, v66, v71
	s_waitcnt lgkmcnt(0)
	v_add_f32_e32 v66, v66, v72
	v_add_f32_e32 v66, v66, v73
	ds_write_b32 v154, v66
	s_waitcnt lgkmcnt(0)
	s_barrier
	s_and_saveexec_b64 s[0:1], s[4:5]
	s_cbranch_execz .LBB0_1513
	ds_read_b128 v[68:71], v157
	ds_read_b128 v[90:93], v157 offset:16
	ds_read_b128 v[94:97], v157 offset:32
	ds_read_b128 v[98:101], v157 offset:48
	ds_read_b128 v[102:105], v157 offset:64
	ds_read_b128 v[106:109], v157 offset:80
	ds_read_b128 v[110:113], v157 offset:96
	ds_read_b128 v[114:117], v157 offset:112
	s_waitcnt lgkmcnt(7)
	v_max_f32_e32 v66, v68, v68
	v_max_f32_e32 v66, 0xff7fc99e, v66
	v_cmp_gt_f32_e32 vcc, v69, v66
	s_nop 1
	v_cndmask_b32_e32 v66, v66, v69, vcc
	v_cndmask_b32_e64 v67, 0, 1, vcc
	v_cmp_gt_f32_e32 vcc, v70, v66
	s_nop 1
	v_cndmask_b32_e32 v66, v66, v70, vcc
	v_cndmask_b32_e64 v67, v67, 2, vcc
	v_cmp_gt_f32_e32 vcc, v71, v66
	s_nop 1
	v_cndmask_b32_e32 v66, v66, v71, vcc
	v_cndmask_b32_e64 v67, v67, 3, vcc
	s_waitcnt lgkmcnt(6)
	v_cmp_gt_f32_e32 vcc, v90, v66
	s_nop 1
	v_cndmask_b32_e32 v66, v66, v90, vcc
	v_cndmask_b32_e64 v67, v67, 4, vcc
	v_cmp_gt_f32_e32 vcc, v91, v66
	s_nop 1
	v_cndmask_b32_e32 v66, v66, v91, vcc
	v_cndmask_b32_e64 v67, v67, 5, vcc
	v_cmp_gt_f32_e32 vcc, v92, v66
	s_nop 1
	v_cndmask_b32_e32 v66, v66, v92, vcc
	v_cndmask_b32_e64 v67, v67, 6, vcc
	v_cmp_gt_f32_e32 vcc, v93, v66
	s_nop 1
	v_cndmask_b32_e32 v66, v66, v93, vcc
	v_cndmask_b32_e64 v67, v67, 7, vcc
	s_waitcnt lgkmcnt(5)
	v_cmp_gt_f32_e32 vcc, v94, v66
	s_nop 1
	v_cndmask_b32_e32 v66, v66, v94, vcc
	v_cndmask_b32_e64 v67, v67, 8, vcc
	v_cmp_gt_f32_e32 vcc, v95, v66
	s_nop 1
	v_cndmask_b32_e32 v66, v66, v95, vcc
	v_cndmask_b32_e64 v67, v67, 9, vcc
	v_cmp_gt_f32_e32 vcc, v96, v66
	s_nop 1
	v_cndmask_b32_e32 v66, v66, v96, vcc
	v_cndmask_b32_e64 v67, v67, 10, vcc
	v_cmp_gt_f32_e32 vcc, v97, v66
	s_nop 1
	v_cndmask_b32_e32 v66, v66, v97, vcc
	v_cndmask_b32_e64 v67, v67, 11, vcc
	s_waitcnt lgkmcnt(4)
	v_cmp_gt_f32_e32 vcc, v98, v66
	s_nop 1
	v_cndmask_b32_e32 v66, v66, v98, vcc
	v_cndmask_b32_e64 v67, v67, 12, vcc
	v_cmp_gt_f32_e32 vcc, v99, v66
	s_nop 1
	v_cndmask_b32_e32 v66, v66, v99, vcc
	v_cndmask_b32_e64 v67, v67, 13, vcc
	v_cmp_gt_f32_e32 vcc, v100, v66
	s_nop 1
	v_cndmask_b32_e32 v66, v66, v100, vcc
	v_cndmask_b32_e64 v67, v67, 14, vcc
	v_cmp_gt_f32_e32 vcc, v101, v66
	s_nop 1
	v_cndmask_b32_e32 v66, v66, v101, vcc
	v_cndmask_b32_e64 v67, v67, 15, vcc
	s_waitcnt lgkmcnt(3)
	v_cmp_gt_f32_e32 vcc, v102, v66
	s_nop 1
	v_cndmask_b32_e32 v66, v66, v102, vcc
	v_cndmask_b32_e64 v67, v67, 16, vcc
	v_cmp_gt_f32_e32 vcc, v103, v66
	s_nop 1
	v_cndmask_b32_e32 v66, v66, v103, vcc
	v_cndmask_b32_e64 v67, v67, 17, vcc
	v_cmp_gt_f32_e32 vcc, v104, v66
	s_nop 1
	v_cndmask_b32_e32 v66, v66, v104, vcc
	v_cndmask_b32_e64 v67, v67, 18, vcc
	v_cmp_gt_f32_e32 vcc, v105, v66
	s_nop 1
	v_cndmask_b32_e32 v66, v66, v105, vcc
	v_cndmask_b32_e64 v67, v67, 19, vcc
	s_waitcnt lgkmcnt(2)
; template <bool SKIP_MIX>
; __device__ __forceinline__ void p8_ln_router(Frame& F0, const In& I) {
;     ...
;             for (int k = 0; k < 4; ++k) { float best = -3.4e38f; int bi = 0;
; #pragma unroll
;                 for (int e = 0; e < 32; ++e) { const bool tk = lv[e] > best; best = tk ? lv[e] : best; bi = tk ? e : bi; }
;                 ti[k] = bi; tv[k] = best;
; #pragma unroll
;                 for (int e = 0; e < 32; ++e) lv[e] = (e == bi) ? -3.4e38f : lv[e]; }
	v_cmp_gt_f32_e32 vcc, v106, v66
	s_nop 1
	v_cndmask_b32_e32 v66, v66, v106, vcc
	v_cndmask_b32_e64 v67, v67, 20, vcc
	v_cmp_gt_f32_e32 vcc, v107, v66
	s_nop 1
	v_cndmask_b32_e32 v66, v66, v107, vcc
	v_cndmask_b32_e64 v67, v67, 21, vcc
	v_cmp_gt_f32_e32 vcc, v108, v66
	s_nop 1
	v_cndmask_b32_e32 v66, v66, v108, vcc
	v_cndmask_b32_e64 v67, v67, 22, vcc
	v_cmp_gt_f32_e32 vcc, v109, v66
	s_nop 1
	v_cndmask_b32_e32 v66, v66, v109, vcc
	v_cndmask_b32_e64 v67, v67, 23, vcc
	s_waitcnt lgkmcnt(1)
	v_cmp_gt_f32_e32 vcc, v110, v66
	s_nop 1
	v_cndmask_b32_e32 v66, v66, v110, vcc
	v_cndmask_b32_e64 v67, v67, 24, vcc
	v_cmp_gt_f32_e32 vcc, v111, v66
	s_nop 1
	v_cndmask_b32_e32 v66, v66, v111, vcc
	v_cndmask_b32_e64 v67, v67, 25, vcc
	v_cmp_gt_f32_e32 vcc, v112, v66
	s_nop 1
	v_cndmask_b32_e32 v66, v66, v112, vcc
	v_cndmask_b32_e64 v67, v67, 26, vcc
	v_cmp_gt_f32_e32 vcc, v113, v66
	s_nop 1
	v_cndmask_b32_e32 v66, v66, v113, vcc
	v_cndmask_b32_e64 v67, v67, 27, vcc
	s_waitcnt lgkmcnt(0)
	v_cmp_gt_f32_e32 vcc, v114, v66
	s_nop 1
	v_cndmask_b32_e32 v66, v66, v114, vcc
	v_cndmask_b32_e64 v67, v67, 28, vcc
	v_cmp_gt_f32_e32 vcc, v115, v66
	s_nop 1
	v_cndmask_b32_e32 v66, v66, v115, vcc
	v_cndmask_b32_e64 v67, v67, 29, vcc
	v_cmp_gt_f32_e32 vcc, v116, v66
	s_nop 1
	v_cndmask_b32_e32 v72, v66, v116, vcc
	v_cndmask_b32_e64 v67, v67, 30, vcc
	v_cmp_gt_f32_e32 vcc, v117, v72
	s_nop 1
	v_cndmask_b32_e64 v66, v67, 31, vcc
	v_cndmask_b32_e32 v73, v72, v117, vcc
	v_cmp_ne_u32_e32 vcc, 0, v66
	s_nop 1
	v_cndmask_b32_e32 v68, v159, v68, vcc
	v_cmp_ne_u32_e32 vcc, 1, v66
	v_max_f32_e32 v67, v68, v68
	v_max_f32_e32 v67, 0xff7fc99e, v67
	v_cndmask_b32_e32 v69, v159, v69, vcc
	v_cmp_ne_u32_e32 vcc, 2, v66
	s_nop 1
	v_cndmask_b32_e32 v70, v159, v70, vcc
	v_cmp_ne_u32_e32 vcc, 3, v66
	s_nop 1
	v_cndmask_b32_e32 v71, v159, v71, vcc
	v_cmp_ne_u32_e32 vcc, 4, v66
	s_nop 1
	v_cndmask_b32_e32 v72, v159, v90, vcc
	v_cmp_ne_u32_e32 vcc, 5, v66
	s_nop 1
	v_cndmask_b32_e32 v90, v159, v91, vcc
	v_cmp_ne_u32_e32 vcc, 6, v66
	s_nop 1
	v_cndmask_b32_e32 v91, v159, v92, vcc
	v_cmp_ne_u32_e32 vcc, 7, v66
	s_nop 1
	v_cndmask_b32_e32 v92, v159, v93, vcc
	v_cmp_ne_u32_e32 vcc, 8, v66
	s_nop 1
	v_cndmask_b32_e32 v93, v159, v94, vcc
	v_cmp_ne_u32_e32 vcc, 9, v66
	s_nop 1
	v_cndmask_b32_e32 v94, v159, v95, vcc
	v_cmp_ne_u32_e32 vcc, 10, v66
	s_nop 1
	v_cndmask_b32_e32 v95, v159, v96, vcc
	v_cmp_ne_u32_e32 vcc, 11, v66
	s_nop 1
	v_cndmask_b32_e32 v96, v159, v97, vcc
	v_cmp_ne_u32_e32 vcc, 12, v66
	s_nop 1
	v_cndmask_b32_e32 v97, v159, v98, vcc
	v_cmp_ne_u32_e32 vcc, 13, v66
	s_nop 1
	v_cndmask_b32_e32 v98, v159, v99, vcc
	v_cmp_ne_u32_e32 vcc, 14, v66
	s_nop 1
	v_cndmask_b32_e32 v99, v159, v100, vcc
	v_cmp_ne_u32_e32 vcc, 15, v66
	s_nop 1
	v_cndmask_b32_e32 v100, v159, v101, vcc
	v_cmp_ne_u32_e32 vcc, 16, v66
	s_nop 1
	v_cndmask_b32_e32 v101, v159, v102, vcc
	v_cmp_ne_u32_e32 vcc, 17, v66
	s_nop 1
	v_cndmask_b32_e32 v102, v159, v103, vcc
	v_cmp_ne_u32_e32 vcc, 18, v66
	s_nop 1
	v_cndmask_b32_e32 v103, v159, v104, vcc
	v_cmp_ne_u32_e32 vcc, 19, v66
	s_nop 1
	v_cndmask_b32_e32 v104, v159, v105, vcc
	v_cmp_ne_u32_e32 vcc, 20, v66
	s_nop 1
	v_cndmask_b32_e32 v105, v159, v106, vcc
	v_cmp_ne_u32_e32 vcc, 21, v66
	s_nop 1
	v_cndmask_b32_e32 v106, v159, v107, vcc
	v_cmp_ne_u32_e32 vcc, 22, v66
	s_nop 1
	v_cndmask_b32_e32 v107, v159, v108, vcc
	v_cmp_ne_u32_e32 vcc, 23, v66
	s_nop 1
	v_cndmask_b32_e32 v108, v159, v109, vcc
	v_cmp_ne_u32_e32 vcc, 24, v66
	s_nop 1
	v_cndmask_b32_e32 v109, v159, v110, vcc
	v_cmp_ne_u32_e32 vcc, 25, v66
	s_nop 1
	v_cndmask_b32_e32 v110, v159, v111, vcc
	v_cmp_ne_u32_e32 vcc, 26, v66
	s_nop 1
	v_cndmask_b32_e32 v111, v159, v112, vcc
	v_cmp_ne_u32_e32 vcc, 27, v66
	s_nop 1
	v_cndmask_b32_e32 v112, v159, v113, vcc
	v_cmp_ne_u32_e32 vcc, 28, v66
	s_nop 1
	v_cndmask_b32_e32 v113, v159, v114, vcc
	v_cmp_ne_u32_e32 vcc, 29, v66
	s_nop 1
	v_cndmask_b32_e32 v114, v159, v115, vcc
	v_cmp_ne_u32_e32 vcc, 30, v66
	s_nop 1
	v_cndmask_b32_e32 v115, v159, v116, vcc
	v_cmp_ne_u32_e32 vcc, 31, v66
	s_nop 1
	v_cndmask_b32_e32 v116, v159, v117, vcc
	v_cmp_gt_f32_e32 vcc, v69, v67
	s_nop 1
	v_cndmask_b32_e32 v67, v67, v69, vcc
	v_cndmask_b32_e64 v117, 0, 1, vcc
	v_cmp_gt_f32_e32 vcc, v70, v67
	s_nop 1
	v_cndmask_b32_e32 v67, v67, v70, vcc
	v_cndmask_b32_e64 v117, v117, 2, vcc
	v_cmp_gt_f32_e32 vcc, v71, v67
	s_nop 1
	v_cndmask_b32_e32 v67, v67, v71, vcc
	v_cndmask_b32_e64 v117, v117, 3, vcc
	v_cmp_gt_f32_e32 vcc, v72, v67
	s_nop 1
	v_cndmask_b32_e32 v67, v67, v72, vcc
	v_cndmask_b32_e64 v117, v117, 4, vcc
	v_cmp_gt_f32_e32 vcc, v90, v67
	s_nop 1
	v_cndmask_b32_e32 v67, v67, v90, vcc
	v_cndmask_b32_e64 v117, v117, 5, vcc
	v_cmp_gt_f32_e32 vcc, v91, v67
	s_nop 1
	v_cndmask_b32_e32 v67, v67, v91, vcc
	v_cndmask_b32_e64 v117, v117, 6, vcc
	v_cmp_gt_f32_e32 vcc, v92, v67
	s_nop 1
	v_cndmask_b32_e32 v67, v67, v92, vcc
	v_cndmask_b32_e64 v117, v117, 7, vcc
	v_cmp_gt_f32_e32 vcc, v93, v67
	s_nop 1
	v_cndmask_b32_e32 v67, v67, v93, vcc
	v_cndmask_b32_e64 v117, v117, 8, vcc
	v_cmp_gt_f32_e32 vcc, v94, v67
	s_nop 1
	v_cndmask_b32_e32 v67, v67, v94, vcc
	v_cndmask_b32_e64 v117, v117, 9, vcc
	v_cmp_gt_f32_e32 vcc, v95, v67
	s_nop 1
	v_cndmask_b32_e32 v67, v67, v95, vcc
	v_cndmask_b32_e64 v117, v117, 10, vcc
	v_cmp_gt_f32_e32 vcc, v96, v67
	s_nop 1
	v_cndmask_b32_e32 v67, v67, v96, vcc
	v_cndmask_b32_e64 v117, v117, 11, vcc
	v_cmp_gt_f32_e32 vcc, v97, v67
	s_nop 1
	v_cndmask_b32_e32 v67, v67, v97, vcc
	v_cndmask_b32_e64 v117, v117, 12, vcc
	v_cmp_gt_f32_e32 vcc, v98, v67
	s_nop 1
	v_cndmask_b32_e32 v67, v67, v98, vcc
	v_cndmask_b32_e64 v117, v117, 13, vcc
	v_cmp_gt_f32_e32 vcc, v99, v67
	s_nop 1
; template <bool SKIP_MIX>
; __device__ __forceinline__ void p8_ln_router(Frame& F0, const In& I) {
;     ...
;             for (int k = 0; k < 4; ++k) { float best = -3.4e38f; int bi = 0;
; #pragma unroll
;                 for (int e = 0; e < 32; ++e) { const bool tk = lv[e] > best; best = tk ? lv[e] : best; bi = tk ? e : bi; }
;                 ti[k] = bi; tv[k] = best;
; #pragma unroll
;                 for (int e = 0; e < 32; ++e) lv[e] = (e == bi) ? -3.4e38f : lv[e]; }
	v_cndmask_b32_e32 v67, v67, v99, vcc
	v_cndmask_b32_e64 v117, v117, 14, vcc
	v_cmp_gt_f32_e32 vcc, v100, v67
	s_nop 1
	v_cndmask_b32_e32 v67, v67, v100, vcc
	v_cndmask_b32_e64 v117, v117, 15, vcc
	v_cmp_gt_f32_e32 vcc, v101, v67
	s_nop 1
	v_cndmask_b32_e32 v67, v67, v101, vcc
	v_cndmask_b32_e64 v117, v117, 16, vcc
	v_cmp_gt_f32_e32 vcc, v102, v67
	s_nop 1
	v_cndmask_b32_e32 v67, v67, v102, vcc
	v_cndmask_b32_e64 v117, v117, 17, vcc
	v_cmp_gt_f32_e32 vcc, v103, v67
	s_nop 1
	v_cndmask_b32_e32 v67, v67, v103, vcc
	v_cndmask_b32_e64 v117, v117, 18, vcc
	v_cmp_gt_f32_e32 vcc, v104, v67
	s_nop 1
	v_cndmask_b32_e32 v67, v67, v104, vcc
	v_cndmask_b32_e64 v117, v117, 19, vcc
	v_cmp_gt_f32_e32 vcc, v105, v67
	s_nop 1
	v_cndmask_b32_e32 v67, v67, v105, vcc
	v_cndmask_b32_e64 v117, v117, 20, vcc
	v_cmp_gt_f32_e32 vcc, v106, v67
	s_nop 1
	v_cndmask_b32_e32 v67, v67, v106, vcc
	v_cndmask_b32_e64 v117, v117, 21, vcc
	v_cmp_gt_f32_e32 vcc, v107, v67
	s_nop 1
	v_cndmask_b32_e32 v67, v67, v107, vcc
	v_cndmask_b32_e64 v117, v117, 22, vcc
	v_cmp_gt_f32_e32 vcc, v108, v67
	s_nop 1
	v_cndmask_b32_e32 v67, v67, v108, vcc
	v_cndmask_b32_e64 v117, v117, 23, vcc
	v_cmp_gt_f32_e32 vcc, v109, v67
	s_nop 1
	v_cndmask_b32_e32 v67, v67, v109, vcc
	v_cndmask_b32_e64 v117, v117, 24, vcc
	v_cmp_gt_f32_e32 vcc, v110, v67
	s_nop 1
	v_cndmask_b32_e32 v67, v67, v110, vcc
	v_cndmask_b32_e64 v117, v117, 25, vcc
	v_cmp_gt_f32_e32 vcc, v111, v67
	s_nop 1
	v_cndmask_b32_e32 v67, v67, v111, vcc
	v_cndmask_b32_e64 v117, v117, 26, vcc
	v_cmp_gt_f32_e32 vcc, v112, v67
	s_nop 1
	v_cndmask_b32_e32 v67, v67, v112, vcc
	v_cndmask_b32_e64 v117, v117, 27, vcc
	v_cmp_gt_f32_e32 vcc, v113, v67
	s_nop 1
	v_cndmask_b32_e32 v67, v67, v113, vcc
	v_cndmask_b32_e64 v117, v117, 28, vcc
	v_cmp_gt_f32_e32 vcc, v114, v67
	s_nop 1
	v_cndmask_b32_e32 v67, v67, v114, vcc
	v_cndmask_b32_e64 v117, v117, 29, vcc
	v_cmp_gt_f32_e32 vcc, v115, v67
	s_nop 1
	v_cndmask_b32_e32 v118, v67, v115, vcc
	v_cndmask_b32_e64 v117, v117, 30, vcc
	v_cmp_gt_f32_e32 vcc, v116, v118
	s_nop 1
	v_cndmask_b32_e64 v67, v117, 31, vcc
	v_cndmask_b32_e32 v117, v118, v116, vcc
	v_cmp_ne_u32_e32 vcc, 0, v67
	s_nop 1
	v_cndmask_b32_e32 v118, v159, v68, vcc
	v_cmp_ne_u32_e32 vcc, 1, v67
	v_max_f32_e32 v68, v118, v118
	v_max_f32_e32 v68, 0xff7fc99e, v68
	v_cndmask_b32_e32 v69, v159, v69, vcc
	v_cmp_ne_u32_e32 vcc, 2, v67
	s_nop 1
	v_cndmask_b32_e32 v70, v159, v70, vcc
	v_cmp_ne_u32_e32 vcc, 3, v67
	s_nop 1
	v_cndmask_b32_e32 v71, v159, v71, vcc
	v_cmp_ne_u32_e32 vcc, 4, v67
	s_nop 1
	v_cndmask_b32_e32 v72, v159, v72, vcc
	v_cmp_ne_u32_e32 vcc, 5, v67
	s_nop 1
	v_cndmask_b32_e32 v90, v159, v90, vcc
	v_cmp_ne_u32_e32 vcc, 6, v67
	s_nop 1
	v_cndmask_b32_e32 v91, v159, v91, vcc
	v_cmp_ne_u32_e32 vcc, 7, v67
	s_nop 1
	v_cndmask_b32_e32 v92, v159, v92, vcc
	v_cmp_ne_u32_e32 vcc, 8, v67
	s_nop 1
	v_cndmask_b32_e32 v93, v159, v93, vcc
	v_cmp_ne_u32_e32 vcc, 9, v67
	s_nop 1
	v_cndmask_b32_e32 v94, v159, v94, vcc
	v_cmp_ne_u32_e32 vcc, 10, v67
	s_nop 1
	v_cndmask_b32_e32 v95, v159, v95, vcc
	v_cmp_ne_u32_e32 vcc, 11, v67
	s_nop 1
	v_cndmask_b32_e32 v96, v159, v96, vcc
	v_cmp_ne_u32_e32 vcc, 12, v67
	s_nop 1
	v_cndmask_b32_e32 v97, v159, v97, vcc
	v_cmp_ne_u32_e32 vcc, 13, v67
	s_nop 1
	v_cndmask_b32_e32 v98, v159, v98, vcc
	v_cmp_ne_u32_e32 vcc, 14, v67
	s_nop 1
	v_cndmask_b32_e32 v99, v159, v99, vcc
	v_cmp_ne_u32_e32 vcc, 15, v67
	s_nop 1
	v_cndmask_b32_e32 v100, v159, v100, vcc
	v_cmp_ne_u32_e32 vcc, 16, v67
	s_nop 1
	v_cndmask_b32_e32 v101, v159, v101, vcc
	v_cmp_ne_u32_e32 vcc, 17, v67
	s_nop 1
	v_cndmask_b32_e32 v102, v159, v102, vcc
	v_cmp_ne_u32_e32 vcc, 18, v67
	s_nop 1
	v_cndmask_b32_e32 v103, v159, v103, vcc
	v_cmp_ne_u32_e32 vcc, 19, v67
	s_nop 1
	v_cndmask_b32_e32 v104, v159, v104, vcc
	v_cmp_ne_u32_e32 vcc, 20, v67
	s_nop 1
	v_cndmask_b32_e32 v105, v159, v105, vcc
	v_cmp_ne_u32_e32 vcc, 21, v67
	s_nop 1
	v_cndmask_b32_e32 v106, v159, v106, vcc
	v_cmp_ne_u32_e32 vcc, 22, v67
	s_nop 1
	v_cndmask_b32_e32 v107, v159, v107, vcc
	v_cmp_ne_u32_e32 vcc, 23, v67
	s_nop 1
	v_cndmask_b32_e32 v108, v159, v108, vcc
	v_cmp_ne_u32_e32 vcc, 24, v67
	s_nop 1
	v_cndmask_b32_e32 v109, v159, v109, vcc
	v_cmp_ne_u32_e32 vcc, 25, v67
	s_nop 1
	v_cndmask_b32_e32 v110, v159, v110, vcc
	v_cmp_ne_u32_e32 vcc, 26, v67
	s_nop 1
	v_cndmask_b32_e32 v111, v159, v111, vcc
	v_cmp_ne_u32_e32 vcc, 27, v67
	s_nop 1
	v_cndmask_b32_e32 v112, v159, v112, vcc
	v_cmp_ne_u32_e32 vcc, 28, v67
	s_nop 1
	v_cndmask_b32_e32 v113, v159, v113, vcc
	v_cmp_ne_u32_e32 vcc, 29, v67
	s_nop 1
	v_cndmask_b32_e32 v114, v159, v114, vcc
	v_cmp_ne_u32_e32 vcc, 30, v67
	s_nop 1
	v_cndmask_b32_e32 v115, v159, v115, vcc
	v_cmp_ne_u32_e32 vcc, 31, v67
	s_nop 1
	v_cndmask_b32_e32 v116, v159, v116, vcc
	v_cmp_gt_f32_e32 vcc, v69, v68
	s_nop 1
	v_cndmask_b32_e32 v68, v68, v69, vcc
	v_cndmask_b32_e64 v119, 0, 1, vcc
	v_cmp_gt_f32_e32 vcc, v70, v68
	s_nop 1
	v_cndmask_b32_e32 v68, v68, v70, vcc
	v_cndmask_b32_e64 v119, v119, 2, vcc
	v_cmp_gt_f32_e32 vcc, v71, v68
	s_nop 1
	v_cndmask_b32_e32 v68, v68, v71, vcc
	v_cndmask_b32_e64 v119, v119, 3, vcc
	v_cmp_gt_f32_e32 vcc, v72, v68
	s_nop 1
	v_cndmask_b32_e32 v68, v68, v72, vcc
	v_cndmask_b32_e64 v119, v119, 4, vcc
	v_cmp_gt_f32_e32 vcc, v90, v68
	s_nop 1
	v_cndmask_b32_e32 v68, v68, v90, vcc
	v_cndmask_b32_e64 v119, v119, 5, vcc
	v_cmp_gt_f32_e32 vcc, v91, v68
	s_nop 1
	v_cndmask_b32_e32 v68, v68, v91, vcc
	v_cndmask_b32_e64 v119, v119, 6, vcc
	v_cmp_gt_f32_e32 vcc, v92, v68
	s_nop 1
	v_cndmask_b32_e32 v68, v68, v92, vcc
	v_cndmask_b32_e64 v119, v119, 7, vcc
	v_cmp_gt_f32_e32 vcc, v93, v68
	s_nop 1
	v_cndmask_b32_e32 v68, v68, v93, vcc
; template <bool SKIP_MIX>
; __device__ __forceinline__ void p8_ln_router(Frame& F0, const In& I) {
;     ...
;             for (int k = 0; k < 4; ++k) { float best = -3.4e38f; int bi = 0;
; #pragma unroll
;                 for (int e = 0; e < 32; ++e) { const bool tk = lv[e] > best; best = tk ? lv[e] : best; bi = tk ? e : bi; }
;                 ti[k] = bi; tv[k] = best;
; #pragma unroll
;                 for (int e = 0; e < 32; ++e) lv[e] = (e == bi) ? -3.4e38f : lv[e]; }
	v_cndmask_b32_e64 v119, v119, 8, vcc
	v_cmp_gt_f32_e32 vcc, v94, v68
	s_nop 1
	v_cndmask_b32_e32 v68, v68, v94, vcc
	v_cndmask_b32_e64 v119, v119, 9, vcc
	v_cmp_gt_f32_e32 vcc, v95, v68
	s_nop 1
	v_cndmask_b32_e32 v68, v68, v95, vcc
	v_cndmask_b32_e64 v119, v119, 10, vcc
	v_cmp_gt_f32_e32 vcc, v96, v68
	s_nop 1
	v_cndmask_b32_e32 v68, v68, v96, vcc
	v_cndmask_b32_e64 v119, v119, 11, vcc
	v_cmp_gt_f32_e32 vcc, v97, v68
	s_nop 1
	v_cndmask_b32_e32 v68, v68, v97, vcc
	v_cndmask_b32_e64 v119, v119, 12, vcc
	v_cmp_gt_f32_e32 vcc, v98, v68
	s_nop 1
	v_cndmask_b32_e32 v68, v68, v98, vcc
	v_cndmask_b32_e64 v119, v119, 13, vcc
	v_cmp_gt_f32_e32 vcc, v99, v68
	s_nop 1
	v_cndmask_b32_e32 v68, v68, v99, vcc
	v_cndmask_b32_e64 v119, v119, 14, vcc
	v_cmp_gt_f32_e32 vcc, v100, v68
	s_nop 1
	v_cndmask_b32_e32 v68, v68, v100, vcc
	v_cndmask_b32_e64 v119, v119, 15, vcc
	v_cmp_gt_f32_e32 vcc, v101, v68
	s_nop 1
	v_cndmask_b32_e32 v68, v68, v101, vcc
	v_cndmask_b32_e64 v119, v119, 16, vcc
	v_cmp_gt_f32_e32 vcc, v102, v68
	s_nop 1
	v_cndmask_b32_e32 v68, v68, v102, vcc
	v_cndmask_b32_e64 v119, v119, 17, vcc
	v_cmp_gt_f32_e32 vcc, v103, v68
	s_nop 1
	v_cndmask_b32_e32 v68, v68, v103, vcc
	v_cndmask_b32_e64 v119, v119, 18, vcc
	v_cmp_gt_f32_e32 vcc, v104, v68
	s_nop 1
	v_cndmask_b32_e32 v68, v68, v104, vcc
	v_cndmask_b32_e64 v119, v119, 19, vcc
	v_cmp_gt_f32_e32 vcc, v105, v68
	s_nop 1
	v_cndmask_b32_e32 v68, v68, v105, vcc
	v_cndmask_b32_e64 v119, v119, 20, vcc
	v_cmp_gt_f32_e32 vcc, v106, v68
	s_nop 1
	v_cndmask_b32_e32 v68, v68, v106, vcc
	v_cndmask_b32_e64 v119, v119, 21, vcc
	v_cmp_gt_f32_e32 vcc, v107, v68
	s_nop 1
	v_cndmask_b32_e32 v68, v68, v107, vcc
	v_cndmask_b32_e64 v119, v119, 22, vcc
	v_cmp_gt_f32_e32 vcc, v108, v68
	s_nop 1
	v_cndmask_b32_e32 v68, v68, v108, vcc
	v_cndmask_b32_e64 v119, v119, 23, vcc
	v_cmp_gt_f32_e32 vcc, v109, v68
	s_nop 1
	v_cndmask_b32_e32 v68, v68, v109, vcc
	v_cndmask_b32_e64 v119, v119, 24, vcc
	v_cmp_gt_f32_e32 vcc, v110, v68
	s_nop 1
	v_cndmask_b32_e32 v68, v68, v110, vcc
	v_cndmask_b32_e64 v119, v119, 25, vcc
	v_cmp_gt_f32_e32 vcc, v111, v68
	s_nop 1
	v_cndmask_b32_e32 v68, v68, v111, vcc
	v_cndmask_b32_e64 v119, v119, 26, vcc
	v_cmp_gt_f32_e32 vcc, v112, v68
	s_nop 1
	v_cndmask_b32_e32 v68, v68, v112, vcc
	v_cndmask_b32_e64 v119, v119, 27, vcc
	v_cmp_gt_f32_e32 vcc, v113, v68
	s_nop 1
	v_cndmask_b32_e32 v68, v68, v113, vcc
	v_cndmask_b32_e64 v119, v119, 28, vcc
	v_cmp_gt_f32_e32 vcc, v114, v68
	s_nop 1
	v_cndmask_b32_e32 v68, v68, v114, vcc
	v_cndmask_b32_e64 v119, v119, 29, vcc
	v_cmp_gt_f32_e32 vcc, v115, v68
	s_nop 1
	v_cndmask_b32_e32 v120, v68, v115, vcc
	v_cndmask_b32_e64 v119, v119, 30, vcc
	v_cmp_gt_f32_e32 vcc, v116, v120
	s_nop 1
	v_cndmask_b32_e64 v68, v119, 31, vcc
	v_cndmask_b32_e32 v119, v120, v116, vcc
	v_cmp_ne_u32_e32 vcc, 0, v68
	s_nop 1
	v_cndmask_b32_e32 v118, v159, v118, vcc
	v_cmp_ne_u32_e32 vcc, 1, v68
	v_max_f32_e32 v118, v118, v118
	v_max_f32_e32 v118, 0xff7fc99e, v118
	v_cndmask_b32_e32 v69, v159, v69, vcc
	v_cmp_ne_u32_e32 vcc, 2, v68
	s_nop 1
	v_cndmask_b32_e32 v70, v159, v70, vcc
	v_cmp_ne_u32_e32 vcc, 3, v68
	s_nop 1
	v_cndmask_b32_e32 v71, v159, v71, vcc
	v_cmp_ne_u32_e32 vcc, 4, v68
	s_nop 1
	v_cndmask_b32_e32 v72, v159, v72, vcc
	v_cmp_ne_u32_e32 vcc, 5, v68
	s_nop 1
	v_cndmask_b32_e32 v90, v159, v90, vcc
	v_cmp_ne_u32_e32 vcc, 6, v68
	s_nop 1
	v_cndmask_b32_e32 v91, v159, v91, vcc
	v_cmp_ne_u32_e32 vcc, 7, v68
	s_nop 1
	v_cndmask_b32_e32 v92, v159, v92, vcc
	v_cmp_ne_u32_e32 vcc, 8, v68
	s_nop 1
	v_cndmask_b32_e32 v93, v159, v93, vcc
	v_cmp_ne_u32_e32 vcc, 9, v68
	s_nop 1
	v_cndmask_b32_e32 v94, v159, v94, vcc
	v_cmp_ne_u32_e32 vcc, 10, v68
	s_nop 1
	v_cndmask_b32_e32 v95, v159, v95, vcc
	v_cmp_ne_u32_e32 vcc, 11, v68
	s_nop 1
	v_cndmask_b32_e32 v96, v159, v96, vcc
	v_cmp_ne_u32_e32 vcc, 12, v68
	s_nop 1
	v_cndmask_b32_e32 v97, v159, v97, vcc
	v_cmp_ne_u32_e32 vcc, 13, v68
	s_nop 1
	v_cndmask_b32_e32 v98, v159, v98, vcc
	v_cmp_ne_u32_e32 vcc, 14, v68
	s_nop 1
	v_cndmask_b32_e32 v99, v159, v99, vcc
	v_cmp_ne_u32_e32 vcc, 15, v68
	s_nop 1
	v_cndmask_b32_e32 v100, v159, v100, vcc
	v_cmp_ne_u32_e32 vcc, 16, v68
	s_nop 1
	v_cndmask_b32_e32 v101, v159, v101, vcc
	v_cmp_ne_u32_e32 vcc, 17, v68
	s_nop 1
	v_cndmask_b32_e32 v102, v159, v102, vcc
	v_cmp_ne_u32_e32 vcc, 18, v68
	s_nop 1
	v_cndmask_b32_e32 v103, v159, v103, vcc
	v_cmp_ne_u32_e32 vcc, 19, v68
	s_nop 1
	v_cndmask_b32_e32 v104, v159, v104, vcc
	v_cmp_ne_u32_e32 vcc, 20, v68
	s_nop 1
	v_cndmask_b32_e32 v105, v159, v105, vcc
	v_cmp_ne_u32_e32 vcc, 21, v68
	s_nop 1
	v_cndmask_b32_e32 v106, v159, v106, vcc
	v_cmp_ne_u32_e32 vcc, 22, v68
	s_nop 1
	v_cndmask_b32_e32 v107, v159, v107, vcc
	v_cmp_ne_u32_e32 vcc, 23, v68
	s_nop 1
	v_cndmask_b32_e32 v108, v159, v108, vcc
	v_cmp_ne_u32_e32 vcc, 24, v68
	s_nop 1
	v_cndmask_b32_e32 v109, v159, v109, vcc
	v_cmp_ne_u32_e32 vcc, 25, v68
	s_nop 1
	v_cndmask_b32_e32 v110, v159, v110, vcc
	v_cmp_ne_u32_e32 vcc, 26, v68
	s_nop 1
	v_cndmask_b32_e32 v111, v159, v111, vcc
	v_cmp_ne_u32_e32 vcc, 27, v68
	s_nop 1
	v_cndmask_b32_e32 v112, v159, v112, vcc
	v_cmp_ne_u32_e32 vcc, 28, v68
	s_nop 1
	v_cndmask_b32_e32 v113, v159, v113, vcc
	v_cmp_ne_u32_e32 vcc, 29, v68
	s_nop 1
	v_cndmask_b32_e32 v114, v159, v114, vcc
	v_cmp_ne_u32_e32 vcc, 30, v68
; #define GAS __attribute__((address_space(1)))
; template <bool SKIP_MIX>
; __device__ __forceinline__ void p8_ln_router(Frame& F0, const In& I) {
;     ...
;             for (int k = 0; k < 4; ++k) { float best = -3.4e38f; int bi = 0;
; #pragma unroll
;                 for (int e = 0; e < 32; ++e) { const bool tk = lv[e] > best; best = tk ? lv[e] : best; bi = tk ? e : bi; }
;                 ti[k] = bi; tv[k] = best;
; #pragma unroll
;                 for (int e = 0; e < 32; ++e) lv[e] = (e == bi) ? -3.4e38f : lv[e]; }
;             float ex[4], sum = 0.f;
; #pragma unroll
;             for (int k = 0; k < 4; ++k) { ex[k] = __expf(tv[k] - tv[0]); sum += ex[k]; }
;             const float inv = 1.f / sum;
;             *(GAS v4u*)((int*)(F.ws + WS_TOPI) + (size_t)(tok0 + tl) * 4) = (v4u){(unsigned)ti[0], (unsigned)ti[1], (unsigned)ti[2], (unsigned)ti[3]};
;             *(GAS f32x4*)((float*)(F.ws + WS_GATE) + (size_t)(tok0 + tl) * 4) = (f32x4){ex[0] * inv, ex[1] * inv, ex[2] * inv, ex[3] * inv};
; #pragma unroll
;             for (int k = 0; k < 4; ++k) __hip_atomic_fetch_add(&hist[ti[k]], 1, __ATOMIC_RELAXED, __HIP_MEMORY_SCOPE_WORKGROUP);
	s_nop 1
	v_cndmask_b32_e32 v115, v159, v115, vcc
	v_cmp_ne_u32_e32 vcc, 31, v68
	s_nop 1
	v_cndmask_b32_e32 v116, v159, v116, vcc
	v_cmp_gt_f32_e32 vcc, v69, v118
	s_nop 1
	v_cndmask_b32_e32 v69, v118, v69, vcc
	v_cndmask_b32_e64 v120, 0, 1, vcc
	v_cmp_gt_f32_e32 vcc, v70, v69
	s_nop 1
	v_cndmask_b32_e32 v69, v69, v70, vcc
	v_cndmask_b32_e64 v118, v120, 2, vcc
	v_cmp_gt_f32_e32 vcc, v71, v69
	s_nop 1
	v_cndmask_b32_e32 v69, v69, v71, vcc
	v_cndmask_b32_e64 v70, v118, 3, vcc
	v_cmp_gt_f32_e32 vcc, v72, v69
	s_nop 1
	v_cndmask_b32_e32 v69, v69, v72, vcc
	v_cndmask_b32_e64 v70, v70, 4, vcc
	v_cmp_gt_f32_e32 vcc, v90, v69
	v_sub_f32_e32 v72, v119, v73
	v_mul_f32_e32 v72, 0x3fb8aa3b, v72
	v_cndmask_b32_e32 v69, v69, v90, vcc
	v_cndmask_b32_e64 v70, v70, 5, vcc
	v_cmp_gt_f32_e32 vcc, v91, v69
	v_exp_f32_e32 v72, v72
	s_nop 0
	v_cndmask_b32_e32 v69, v69, v91, vcc
	v_cndmask_b32_e64 v70, v70, 6, vcc
	v_cmp_gt_f32_e32 vcc, v92, v69
	s_nop 1
	v_cndmask_b32_e32 v69, v69, v92, vcc
	v_cndmask_b32_e64 v70, v70, 7, vcc
	v_cmp_gt_f32_e32 vcc, v93, v69
	s_nop 1
	v_cndmask_b32_e32 v69, v69, v93, vcc
	v_cndmask_b32_e64 v70, v70, 8, vcc
	v_cmp_gt_f32_e32 vcc, v94, v69
	s_nop 1
	v_cndmask_b32_e32 v69, v69, v94, vcc
	v_cndmask_b32_e64 v70, v70, 9, vcc
	v_cmp_gt_f32_e32 vcc, v95, v69
	s_nop 1
	v_cndmask_b32_e32 v69, v69, v95, vcc
	v_cndmask_b32_e64 v70, v70, 10, vcc
	v_cmp_gt_f32_e32 vcc, v96, v69
	s_nop 1
	v_cndmask_b32_e32 v69, v69, v96, vcc
	v_cndmask_b32_e64 v70, v70, 11, vcc
	v_cmp_gt_f32_e32 vcc, v97, v69
	s_nop 1
	v_cndmask_b32_e32 v69, v69, v97, vcc
	v_cndmask_b32_e64 v70, v70, 12, vcc
	v_cmp_gt_f32_e32 vcc, v98, v69
	s_nop 1
	v_cndmask_b32_e32 v69, v69, v98, vcc
	v_cndmask_b32_e64 v70, v70, 13, vcc
	v_cmp_gt_f32_e32 vcc, v99, v69
	s_nop 1
	v_cndmask_b32_e32 v69, v69, v99, vcc
	v_cndmask_b32_e64 v70, v70, 14, vcc
	v_cmp_gt_f32_e32 vcc, v100, v69
	s_nop 1
	v_cndmask_b32_e32 v69, v69, v100, vcc
	v_cndmask_b32_e64 v70, v70, 15, vcc
	v_cmp_gt_f32_e32 vcc, v101, v69
	s_nop 1
	v_cndmask_b32_e32 v69, v69, v101, vcc
	v_cndmask_b32_e64 v70, v70, 16, vcc
	v_cmp_gt_f32_e32 vcc, v102, v69
	s_nop 1
	v_cndmask_b32_e32 v69, v69, v102, vcc
	v_cndmask_b32_e64 v70, v70, 17, vcc
	v_cmp_gt_f32_e32 vcc, v103, v69
	s_nop 1
	v_cndmask_b32_e32 v69, v69, v103, vcc
	v_cndmask_b32_e64 v70, v70, 18, vcc
	v_cmp_gt_f32_e32 vcc, v104, v69
	s_nop 1
	v_cndmask_b32_e32 v69, v69, v104, vcc
	v_cndmask_b32_e64 v70, v70, 19, vcc
	v_cmp_gt_f32_e32 vcc, v105, v69
	s_nop 1
	v_cndmask_b32_e32 v69, v69, v105, vcc
	v_cndmask_b32_e64 v70, v70, 20, vcc
	v_cmp_gt_f32_e32 vcc, v106, v69
	s_nop 1
	v_cndmask_b32_e32 v69, v69, v106, vcc
	v_cndmask_b32_e64 v70, v70, 21, vcc
	v_cmp_gt_f32_e32 vcc, v107, v69
	s_nop 1
	v_cndmask_b32_e32 v69, v69, v107, vcc
	v_cndmask_b32_e64 v70, v70, 22, vcc
	v_cmp_gt_f32_e32 vcc, v108, v69
	s_nop 1
	v_cndmask_b32_e32 v69, v69, v108, vcc
	v_cndmask_b32_e64 v70, v70, 23, vcc
	v_cmp_gt_f32_e32 vcc, v109, v69
	s_nop 1
	v_cndmask_b32_e32 v69, v69, v109, vcc
	v_cndmask_b32_e64 v70, v70, 24, vcc
	v_cmp_gt_f32_e32 vcc, v110, v69
	s_nop 1
	v_cndmask_b32_e32 v69, v69, v110, vcc
	v_cndmask_b32_e64 v70, v70, 25, vcc
	v_cmp_gt_f32_e32 vcc, v111, v69
	s_nop 1
	v_cndmask_b32_e32 v69, v69, v111, vcc
	v_cndmask_b32_e64 v70, v70, 26, vcc
	v_cmp_gt_f32_e32 vcc, v112, v69
	s_nop 1
	v_cndmask_b32_e32 v69, v69, v112, vcc
	v_cndmask_b32_e64 v70, v70, 27, vcc
	v_cmp_gt_f32_e32 vcc, v113, v69
	s_nop 1
	v_cndmask_b32_e32 v69, v69, v113, vcc
	v_cndmask_b32_e64 v70, v70, 28, vcc
	v_cmp_gt_f32_e32 vcc, v114, v69
	s_nop 1
	v_cndmask_b32_e32 v69, v69, v114, vcc
	v_cndmask_b32_e64 v70, v70, 29, vcc
	v_cmp_gt_f32_e32 vcc, v115, v69
	s_nop 1
	v_cndmask_b32_e32 v71, v69, v115, vcc
	v_cndmask_b32_e64 v70, v70, 30, vcc
	v_cmp_gt_f32_e32 vcc, v116, v71
	s_nop 1
	v_cndmask_b32_e64 v69, v70, 31, vcc
	v_sub_f32_e32 v70, v73, v73
	v_cndmask_b32_e32 v90, v71, v116, vcc
	v_mul_f32_e32 v70, 0x3fb8aa3b, v70
	v_sub_f32_e32 v71, v117, v73
	v_exp_f32_e32 v70, v70
	v_mul_f32_e32 v71, 0x3fb8aa3b, v71
	v_exp_f32_e32 v71, v71
	v_sub_f32_e32 v73, v90, v73
	v_mul_f32_e32 v73, 0x3fb8aa3b, v73
	v_exp_f32_e32 v73, v73
	v_add_f32_e32 v90, 0, v70
	v_add_f32_e32 v90, v90, v71
	v_add_f32_e32 v90, v90, v72
	v_add_f32_e32 v90, v90, v73
	v_div_scale_f32 v91, s[14:15], v90, v90, 1.0
	v_rcp_f32_e32 v92, v91
	s_nop 0
	v_fma_f32 v93, -v91, v92, 1.0
	v_fmac_f32_e32 v92, v93, v92
	v_div_scale_f32 v93, vcc, 1.0, v90, 1.0
	v_mul_f32_e32 v94, v93, v92
	v_fma_f32 v95, -v91, v94, v93
	v_fmac_f32_e32 v94, v95, v92
	v_fma_f32 v91, -v91, v94, v93
	v_div_fmas_f32 v91, v91, v92, v94
	v_add_u32_e32 v92, s23, v74
	v_ashrrev_i32_e32 v93, 31, v92
	v_div_fixup_f32 v90, v91, v90, 1.0
	v_lshlrev_b64 v[92:93], 4, v[92:93]
	v_lshl_add_u64 v[94:95], s[6:7], 0, v[92:93]
	v_pk_mul_f32 v[72:73], v[72:73], v[90:91] op_sel_hi:[1,0]
	v_pk_mul_f32 v[70:71], v[70:71], v[90:91] op_sel_hi:[1,0]
	v_lshl_add_u64 v[90:91], s[10:11], 0, v[92:93]
	global_store_dwordx4 v[94:95], v[66:69], off
	global_store_dwordx4 v[90:91], v[70:73], off
	s_nop 0
	v_lshl_add_u32 v66, v66, 2, s21
	ds_add_u32 v66, v158
	v_lshl_add_u32 v66, v67, 2, s21
	ds_add_u32 v66, v158
	v_lshl_add_u32 v66, v68, 2, s21
	ds_add_u32 v66, v158
	v_lshl_add_u32 v66, v69, 2, s21
	ds_add_u32 v66, v158
	s_branch .LBB0_1513

;     __device__ __forceinline__ bool next(int i, Unit& u) const { u.aux = 0; return t.map(i, u.pm, u.pn); }
;     __device__ __forceinline__ bool next(int i, Unit& u) const { u.aux = i & 1; return t.map(i >> 1, u.pm, u.pn); }
; #define PG8_STAGE(bufoff, goff, voff) do { _Pragma("unroll") for (int _i = 0; _i < 2; ++_i) \
;         __builtin_amdgcn_raw_ptr_buffer_load_lds(rsrc, (PG8_LAS void*)(lds + (bufoff) + ldsw + _i * 8192), 16, (int)(voff), (int)((goff) + _i * p1##voff), 0, 0); } while (0)
; #define PG8_LDA(dst, b, h) do { _Pragma("unroll") for (int m = 0; m < 4; ++m) dst[m] = PG8_LD8(lds + PG8_SA(b, h) + aoff + m * 2048); } while (0)
; #define PG8_WAIT_V(n) asm volatile("s_waitcnt vmcnt(" #n ")" ::: "memory")
; template <class Epi, class Sched, bool ALIGN_EPI, bool F8 = false, int F8SC = F8_SCALES>
; __device__ __forceinline__ void gemm_phase(PG8_LAS unsigned char* lds, const __amdgpu_buffer_rsrc_t rsrc, const int lda, const int ldb, const int K, const Sched& S, const Epi& E) {
;     ...
;     Unit cur, nxt; int ui = 0;
;     if (!S.next(0, cur)) return;
;     f32x4 acc[2][2][4][2];
;     PG8_ZERO();
;     i32x8 At[4], B0[2], B1[2];
;     unsigned cA, cB; S.bases(cur, cA, cB); cA = __builtin_amdgcn_readfirstlane(cA); cB = __builtin_amdgcn_readfirstlane(cB);
;     PG8_STAGE(PG8_SB(0, 0), cB, voffB); PG8_STAGE(PG8_SB(0, 1), cB + hsB, voffB); PG8_STAGE(PG8_SA(0, 0), cA, voffA); PG8_STAGE(PG8_SA(0, 1), cA + hsA, voffA);
;     if (wr == 1) PG8_BAR;
;     PG8_WAIT_V(2); PG8_BAR;
;     PG8_STAGE(PG8_SB(1, 0), cB + kstep, voffB); PG8_STAGE(PG8_SA(1, 0), cA + kstep, voffA); PG8_STAGE(PG8_SB(1, 1), cB + hsB + kstep, voffB);
;     PG8_WAIT_V(6); PG8_BAR;
;     for (;;) {
;         const bool has_next = S.next(ui + 1, nxt);
;         unsigned nA = cA, nB = cB; if (has_next) { S.bases(nxt, nA, nB); nA = __builtin_amdgcn_readfirstlane(nA); nB = __builtin_amdgcn_readfirstlane(nB); }
; #pragma unroll 1
;         for (int t = 0; t < nt; t += 2) {
;             const bool last = (t == nt - 2);
;             const unsigned a1 = cA + (unsigned)(t + 1) * kstep;
;             const unsigned a2 = last ? nA : cA + (unsigned)(t + 2) * kstep, b2 = last ? nB : cB + (unsigned)(t + 2) * kstep;
;             const unsigned a3 = a2 + kstep, b3 = b2 + kstep;
;             PG8_LDB(B0, 0, 0); PG8_LDB(B1, 0, 1); PG8_SCHED; PG8_LDA(At, 0, 0); PG8_STAGE(PG8_SA(1, 1), a1 + hsA, voffA);
.LBB0_1724:
	v_mov_b32_e32 v2, 0
	s_add_i32 s4, s50, 0x60080
	s_add_i32 s5, s49, 0x100
	s_mov_b32 s49, -2
	v_mov_b32_e32 v3, v2
	v_mov_b32_e32 v4, v2
	v_mov_b32_e32 v5, v2
	v_mov_b32_e32 v6, v2
	v_mov_b32_e32 v7, v2
	v_mov_b32_e32 v8, v2
	v_mov_b32_e32 v9, v2
	s_waitcnt vmcnt(25)
	v_mov_b32_e32 v18, v2
	v_mov_b32_e32 v19, v2
	v_mov_b32_e32 v20, v2
	v_mov_b32_e32 v21, v2
	s_waitcnt vmcnt(24)
	v_mov_b32_e32 v22, v2
	v_mov_b32_e32 v23, v2
	v_mov_b32_e32 v24, v2
	v_mov_b32_e32 v25, v2
	s_waitcnt vmcnt(21)
	v_mov_b32_e32 v34, v2
	v_mov_b32_e32 v35, v2
	v_mov_b32_e32 v36, v2
	v_mov_b32_e32 v37, v2
	s_waitcnt vmcnt(20)
	v_mov_b32_e32 v38, v2
	v_mov_b32_e32 v39, v2
	v_mov_b32_e32 v40, v2
	v_mov_b32_e32 v41, v2
	s_waitcnt vmcnt(17)
	v_mov_b32_e32 v50, v2
	v_mov_b32_e32 v51, v2
	v_mov_b32_e32 v52, v2
	v_mov_b32_e32 v53, v2
	s_waitcnt vmcnt(16)
	v_mov_b32_e32 v54, v2
	v_mov_b32_e32 v55, v2
	v_mov_b32_e32 v56, v2
	v_mov_b32_e32 v57, v2
	v_mov_b32_e32 v10, v2
	v_mov_b32_e32 v11, v2
	v_mov_b32_e32 v12, v2
	v_mov_b32_e32 v13, v2
	v_mov_b32_e32 v14, v2
	v_mov_b32_e32 v15, v2
	v_mov_b32_e32 v16, v2
	v_mov_b32_e32 v17, v2
	v_mov_b32_e32 v26, v2
	v_mov_b32_e32 v27, v2
	v_mov_b32_e32 v28, v2
	v_mov_b32_e32 v29, v2
	v_mov_b32_e32 v30, v2
	v_mov_b32_e32 v31, v2
	v_mov_b32_e32 v32, v2
	v_mov_b32_e32 v33, v2
	v_mov_b32_e32 v42, v2
	v_mov_b32_e32 v43, v2
	v_mov_b32_e32 v44, v2
	v_mov_b32_e32 v45, v2
	v_mov_b32_e32 v46, v2
	v_mov_b32_e32 v47, v2
	v_mov_b32_e32 v48, v2
	v_mov_b32_e32 v49, v2
	s_waitcnt vmcnt(15)
	v_mov_b32_e32 v58, v2
	v_mov_b32_e32 v59, v2
	v_mov_b32_e32 v60, v2
	v_mov_b32_e32 v61, v2
	s_waitcnt vmcnt(14)
	v_mov_b32_e32 v62, v2
	v_mov_b32_e32 v63, v2
	v_mov_b32_e32 v64, v2
	v_mov_b32_e32 v65, v2
	v_mov_b32_e32 v66, v2
	v_mov_b32_e32 v67, v2
	v_mov_b32_e32 v68, v2
	v_mov_b32_e32 v69, v2
	v_mov_b32_e32 v70, v2
	v_mov_b32_e32 v71, v2
	v_mov_b32_e32 v72, v2
	v_mov_b32_e32 v73, v2
	v_mov_b32_e32 v82, v2
	v_mov_b32_e32 v83, v2
	v_mov_b32_e32 v84, v2
	v_mov_b32_e32 v85, v2
	v_mov_b32_e32 v86, v2
	v_mov_b32_e32 v87, v2
	v_mov_b32_e32 v88, v2
	v_mov_b32_e32 v89, v2
	v_mov_b32_e32 v98, v2
	v_mov_b32_e32 v99, v2
	v_mov_b32_e32 v100, v2
	v_mov_b32_e32 v101, v2
	v_mov_b32_e32 v102, v2
	v_mov_b32_e32 v103, v2
	v_mov_b32_e32 v104, v2
	v_mov_b32_e32 v105, v2
	v_mov_b32_e32 v114, v2
	v_mov_b32_e32 v115, v2
	v_mov_b32_e32 v116, v2
	v_mov_b32_e32 v117, v2
	v_mov_b32_e32 v118, v2
	v_mov_b32_e32 v119, v2
	v_mov_b32_e32 v120, v2
	v_mov_b32_e32 v121, v2
	v_mov_b32_e32 v74, v2
	v_mov_b32_e32 v75, v2
	v_mov_b32_e32 v76, v2
	v_mov_b32_e32 v77, v2
	v_mov_b32_e32 v78, v2
	v_mov_b32_e32 v79, v2
	v_mov_b32_e32 v80, v2
	v_mov_b32_e32 v81, v2
	v_mov_b32_e32 v90, v2
	v_mov_b32_e32 v91, v2
	v_mov_b32_e32 v92, v2
	v_mov_b32_e32 v93, v2
	v_mov_b32_e32 v94, v2
	v_mov_b32_e32 v95, v2
	v_mov_b32_e32 v96, v2
	v_mov_b32_e32 v97, v2
	v_mov_b32_e32 v106, v2
	v_mov_b32_e32 v107, v2
	v_mov_b32_e32 v108, v2
	v_mov_b32_e32 v109, v2
	v_mov_b32_e32 v110, v2
	v_mov_b32_e32 v111, v2
	v_mov_b32_e32 v112, v2
	v_mov_b32_e32 v113, v2
	v_mov_b32_e32 v122, v2
	v_mov_b32_e32 v123, v2
	v_mov_b32_e32 v124, v2
	v_mov_b32_e32 v125, v2
	v_mov_b32_e32 v126, v2
	v_mov_b32_e32 v127, v2
	v_mov_b32_e32 v128, v2
	v_mov_b32_e32 v129, v2
.LBB0_1725:
	ds_read_b128 v[130:133], v169
	ds_read_b128 v[134:137], v169 offset:1024
	ds_read_b128 v[138:141], v169 offset:2048
	ds_read_b128 v[142:145], v169 offset:3072
	ds_read_b128 v[150:153], v170
	ds_read_b128 v[154:157], v170 offset:1024
	ds_read_b128 v[158:161], v170 offset:2048
	ds_read_b128 v[162:165], v170 offset:3072
	s_add_i32 s50, s4, 0xfffa0080
	s_cmp_eq_u32 s49, 12
	s_cselect_b32 s50, s47, s50
	s_cselect_b32 s52, s46, s5
	s_add_i32 s51, s50, 0x80
	s_add_i32 s53, s4, 0xfffe0000
	s_mov_b32 s80, s96
	s_mov_b32 m0, s30
	ds_read_b128 v[176:179], v171
	ds_read_b128 v[180:183], v171 offset:1024
	ds_read_b128 v[184:187], v171 offset:2048
	ds_read_b128 v[188:191], v171 offset:3072
	ds_read_b128 v[192:195], v171 offset:4096
	ds_read_b128 v[196:199], v171 offset:5120
	ds_read_b128 v[200:203], v171 offset:6144
	ds_read_b128 v[204:207], v171 offset:7168
	buffer_load_dwordx4 v1, s[80:83], s53 offen lds
	s_mov_b32 m0, s31
	s_nop 0
	buffer_load_dwordx4 v1, s[80:83], s4 offen lds
	s_waitcnt vmcnt(8)
	s_waitcnt lgkmcnt(0)
	s_barrier
	s_setprio 1
	s_waitcnt lgkmcnt(6)
	v_mfma_scale_f32_16x16x128_f8f6f4 v[126:129], v[130:137], v[176:183], v[126:129], v172, v172 op_sel:[0,1,0] op_sel_hi:[0,0,0]
	v_mfma_scale_f32_16x16x128_f8f6f4 v[122:125], v[138:145], v[176:183], v[122:125], v172, v172 op_sel:[0,1,0] op_sel_hi:[0,0,0]
	s_waitcnt lgkmcnt(4)
	v_mfma_scale_f32_16x16x128_f8f6f4 v[110:113], v[130:137], v[184:191], v[110:113], v172, v172 op_sel:[0,1,0] op_sel_hi:[0,0,0]
	v_mfma_scale_f32_16x16x128_f8f6f4 v[106:109], v[138:145], v[184:191], v[106:109], v172, v172 op_sel:[0,1,0] op_sel_hi:[0,0,0]
	s_waitcnt lgkmcnt(2)
	v_mfma_scale_f32_16x16x128_f8f6f4 v[208:211], v[130:137], v[192:199], v[94:97], v172, v172 op_sel:[0,1,0] op_sel_hi:[0,0,0]
	v_mfma_scale_f32_16x16x128_f8f6f4 v[212:215], v[138:145], v[192:199], v[90:93], v172, v172 op_sel:[0,1,0] op_sel_hi:[0,0,0]
	s_waitcnt lgkmcnt(0)
	v_mfma_scale_f32_16x16x128_f8f6f4 v[216:219], v[130:137], v[200:207], v[78:81], v172, v172 op_sel:[0,1,0] op_sel_hi:[0,0,0]
	v_mfma_scale_f32_16x16x128_f8f6f4 v[220:223], v[138:145], v[200:207], v[74:77], v172, v172 op_sel:[0,1,0] op_sel_hi:[0,0,0]
	s_setprio 0
	s_setprio 1
	v_mfma_scale_f32_16x16x128_f8f6f4 v[118:121], v[150:157], v[176:183], v[118:121], v172, v172 op_sel:[0,1,0] op_sel_hi:[0,0,0]
	v_mfma_scale_f32_16x16x128_f8f6f4 v[114:117], v[158:165], v[176:183], v[114:117], v172, v172 op_sel:[0,1,0] op_sel_hi:[0,0,0]
	v_mfma_scale_f32_16x16x128_f8f6f4 v[102:105], v[150:157], v[184:191], v[102:105], v172, v172 op_sel:[0,1,0] op_sel_hi:[0,0,0]
	v_mfma_scale_f32_16x16x128_f8f6f4 v[98:101], v[158:165], v[184:191], v[98:101], v172, v172 op_sel:[0,1,0] op_sel_hi:[0,0,0]
	v_mfma_scale_f32_16x16x128_f8f6f4 v[176:179], v[150:157], v[192:199], v[86:89], v172, v172 op_sel:[0,1,0] op_sel_hi:[0,0,0]
	v_mfma_scale_f32_16x16x128_f8f6f4 v[180:183], v[158:165], v[192:199], v[82:85], v172, v172 op_sel:[0,1,0] op_sel_hi:[0,0,0]
	v_mfma_scale_f32_16x16x128_f8f6f4 v[184:187], v[150:157], v[200:207], v[70:73], v172, v172 op_sel:[0,1,0] op_sel_hi:[0,0,0]
	v_mfma_scale_f32_16x16x128_f8f6f4 v[188:191], v[158:165], v[200:207], v[66:69], v172, v172 op_sel:[0,1,0] op_sel_hi:[0,0,0]
	s_setprio 0
	s_barrier
; #define PG8_STAGE(bufoff, goff, voff) do { _Pragma("unroll") for (int _i = 0; _i < 2; ++_i) \
;         __builtin_amdgcn_raw_ptr_buffer_load_lds(rsrc, (PG8_LAS void*)(lds + (bufoff) + ldsw + _i * 8192), 16, (int)(voff), (int)((goff) + _i * p1##voff), 0, 0); } while (0)
; #define PG8_LDA(dst, b, h) do { _Pragma("unroll") for (int m = 0; m < 4; ++m) dst[m] = PG8_LD8(lds + PG8_SA(b, h) + aoff + m * 2048); } while (0)
; #define PG8_LDB(dst, b, h) do { _Pragma("unroll") for (int n = 0; n < 2; ++n) dst[n] = PG8_LD8(lds + PG8_SB(b, h) + boff + n * 2048); } while (0)
; #define PG8_WAIT_V(n) asm volatile("s_waitcnt vmcnt(" #n ")" ::: "memory")
; #define PG8_WAIT_L(n) asm volatile("s_waitcnt lgkmcnt(" #n ")" ::: "memory")
; #define PG8_BAR __builtin_amdgcn_s_barrier()
; #define PG8_SCHED __builtin_amdgcn_sched_barrier(0)
; template <class Epi, class Sched, bool ALIGN_EPI, bool F8 = false, int F8SC = F8_SCALES>
; __device__ __forceinline__ void gemm_phase(PG8_LAS unsigned char* lds, const __amdgpu_buffer_rsrc_t rsrc, const int lda, const int ldb, const int K, const Sched& S, const Epi& E) {
;     ...
;             PG8_LDA(At, 0, 1); PG8_STAGE(PG8_SB(0, 0), b2, voffB); PG8_STAGE(PG8_SB(0, 1), b2 + hsB, voffB); PG8_STAGE(PG8_SA(0, 0), a2, voffA);
;             PG8_WAIT_V(8); PG8_WAIT_L(0); PG8_BAR; PG8_MMA(1, 0, At, B0); PG8_MMA(1, 1, At, B1); PG8_BAR; PG8_SCHED;
;             PG8_LDB(B0, 1, 0); PG8_LDB(B1, 1, 1); PG8_SCHED; PG8_LDA(At, 1, 0); PG8_STAGE(PG8_SA(0, 1), a2 + hsA, voffA);
;             PG8_WAIT_V(8); PG8_WAIT_L(0); PG8_BAR; PG8_MMA(0, 0, At, B0); PG8_MMA(0, 1, At, B1); PG8_BAR; PG8_SCHED;
;             PG8_LDA(At, 1, 1); PG8_STAGE(PG8_SB(1, 0), b3, voffB); PG8_STAGE(PG8_SB(1, 1), b3 + hsB, voffB); PG8_STAGE(PG8_SA(1, 0), a3, voffA);
	s_mov_b32 m0, s16
	s_nop 3
	ds_read_b128 v[66:69], v171 offset:16384
	ds_read_b128 v[70:73], v171 offset:17408
	ds_read_b128 v[74:77], v171 offset:18432
	ds_read_b128 v[78:81], v171 offset:19456
	ds_read_b128 v[82:85], v171 offset:20480
	ds_read_b128 v[86:89], v171 offset:21504
	ds_read_b128 v[90:93], v171 offset:22528
	ds_read_b128 v[94:97], v171 offset:23552
	buffer_load_dwordx4 v168, s[80:83], s52 offen lds
	s_add_i32 s53, s52, 0x20000
	s_mov_b32 m0, s17
	s_nop 0
	buffer_load_dwordx4 v168, s[80:83], s53 offen lds
	s_add_i32 s53, s52, 0x40000
	s_mov_b32 m0, s18
	s_nop 0
	buffer_load_dwordx4 v168, s[80:83], s53 offen lds
	s_add_i32 s53, s52, 0x60000
	s_mov_b32 m0, s19
	s_nop 0
	buffer_load_dwordx4 v168, s[80:83], s53 offen lds
	s_mov_b32 m0, s15
	s_add_i32 s53, s50, 0x20000
	buffer_load_dwordx4 v1, s[80:83], s50 offen lds
	s_mov_b32 m0, s20
	s_nop 0
	buffer_load_dwordx4 v1, s[80:83], s53 offen lds
	s_waitcnt vmcnt(8)
	s_waitcnt lgkmcnt(0)
	s_barrier
	s_setprio 1
	s_waitcnt lgkmcnt(6)
	v_mfma_scale_f32_16x16x128_f8f6f4 v[62:65], v[130:137], v[66:73], v[62:65], v172, v172 op_sel:[0,1,0] op_sel_hi:[0,0,0]
	v_mfma_scale_f32_16x16x128_f8f6f4 v[58:61], v[138:145], v[66:73], v[58:61], v172, v172 op_sel:[0,1,0] op_sel_hi:[0,0,0]
	s_waitcnt lgkmcnt(4)
	v_mfma_scale_f32_16x16x128_f8f6f4 v[192:195], v[130:137], v[74:81], v[46:49], v172, v172 op_sel:[0,1,0] op_sel_hi:[0,0,0]
	v_mfma_scale_f32_16x16x128_f8f6f4 v[196:199], v[138:145], v[74:81], v[42:45], v172, v172 op_sel:[0,1,0] op_sel_hi:[0,0,0]
	s_waitcnt lgkmcnt(2)
	v_mfma_scale_f32_16x16x128_f8f6f4 v[200:203], v[130:137], v[82:89], v[30:33], v172, v172 op_sel:[0,1,0] op_sel_hi:[0,0,0]
	v_mfma_scale_f32_16x16x128_f8f6f4 v[204:207], v[138:145], v[82:89], v[26:29], v172, v172 op_sel:[0,1,0] op_sel_hi:[0,0,0]
	s_waitcnt lgkmcnt(0)
	v_mfma_scale_f32_16x16x128_f8f6f4 v[224:227], v[130:137], v[90:97], v[14:17], v172, v172 op_sel:[0,1,0] op_sel_hi:[0,0,0]
	v_mfma_scale_f32_16x16x128_f8f6f4 v[228:231], v[138:145], v[90:97], v[10:13], v172, v172 op_sel:[0,1,0] op_sel_hi:[0,0,0]
	s_setprio 0
	s_setprio 1
	v_mfma_scale_f32_16x16x128_f8f6f4 v[54:57], v[150:157], v[66:73], v[54:57], v172, v172 op_sel:[0,1,0] op_sel_hi:[0,0,0]
	v_mfma_scale_f32_16x16x128_f8f6f4 v[50:53], v[158:165], v[66:73], v[50:53], v172, v172 op_sel:[0,1,0] op_sel_hi:[0,0,0]
	v_mfma_scale_f32_16x16x128_f8f6f4 v[232:235], v[150:157], v[74:81], v[38:41], v172, v172 op_sel:[0,1,0] op_sel_hi:[0,0,0]
	v_mfma_scale_f32_16x16x128_f8f6f4 v[236:239], v[158:165], v[74:81], v[34:37], v172, v172 op_sel:[0,1,0] op_sel_hi:[0,0,0]
	v_mfma_scale_f32_16x16x128_f8f6f4 v[240:243], v[150:157], v[82:89], v[22:25], v172, v172 op_sel:[0,1,0] op_sel_hi:[0,0,0]
	v_mfma_scale_f32_16x16x128_f8f6f4 v[244:247], v[158:165], v[82:89], v[18:21], v172, v172 op_sel:[0,1,0] op_sel_hi:[0,0,0]
	v_mfma_scale_f32_16x16x128_f8f6f4 v[248:251], v[150:157], v[90:97], v[6:9], v172, v172 op_sel:[0,1,0] op_sel_hi:[0,0,0]
	v_mfma_scale_f32_16x16x128_f8f6f4 v[146:149], v[158:165], v[90:97], v[2:5], v172, v172 op_sel:[0,1,0] op_sel_hi:[0,0,0]
	s_setprio 0
	s_barrier
	s_nop 4
	ds_read_b128 v[2:5], v173
	ds_read_b128 v[6:9], v173 offset:1024
	ds_read_b128 v[18:21], v173 offset:2048
	ds_read_b128 v[22:25], v173 offset:3072
	ds_read_b128 v[130:133], v174
	ds_read_b128 v[134:137], v174 offset:1024
	ds_read_b128 v[138:141], v174 offset:2048
	ds_read_b128 v[142:145], v174 offset:3072
	s_mov_b32 m0, s21
	s_add_i32 s53, s50, 0x40000
	ds_read_b128 v[10:13], v171 offset:32768
	ds_read_b128 v[14:17], v171 offset:33792
	ds_read_b128 v[26:29], v171 offset:34816
	ds_read_b128 v[30:33], v171 offset:35840
	ds_read_b128 v[34:37], v171 offset:36864
	ds_read_b128 v[38:41], v171 offset:37888
	ds_read_b128 v[42:45], v171 offset:38912
	ds_read_b128 v[46:49], v171 offset:39936
	buffer_load_dwordx4 v1, s[80:83], s53 offen lds
	s_add_i32 s53, s50, 0x60000
	s_mov_b32 m0, s22
	s_nop 0
	buffer_load_dwordx4 v1, s[80:83], s53 offen lds
	s_waitcnt vmcnt(8)
	s_waitcnt lgkmcnt(0)
	s_barrier
	s_setprio 1
	s_waitcnt lgkmcnt(6)
	v_mfma_scale_f32_16x16x128_f8f6f4 v[126:129], v[2:9], v[10:17], v[126:129], v172, v172 op_sel:[0,1,0] op_sel_hi:[0,0,0]
	v_mfma_scale_f32_16x16x128_f8f6f4 v[122:125], v[18:25], v[10:17], v[122:125], v172, v172 op_sel:[0,1,0] op_sel_hi:[0,0,0]
	s_waitcnt lgkmcnt(4)
	v_mfma_scale_f32_16x16x128_f8f6f4 v[110:113], v[2:9], v[26:33], v[110:113], v172, v172 op_sel:[0,1,0] op_sel_hi:[0,0,0]
	v_mfma_scale_f32_16x16x128_f8f6f4 v[106:109], v[18:25], v[26:33], v[106:109], v172, v172 op_sel:[0,1,0] op_sel_hi:[0,0,0]
	s_waitcnt lgkmcnt(2)
	v_mfma_scale_f32_16x16x128_f8f6f4 v[94:97], v[2:9], v[34:41], v[208:211], v172, v172 op_sel:[0,1,0] op_sel_hi:[0,0,0]
	v_mfma_scale_f32_16x16x128_f8f6f4 v[90:93], v[18:25], v[34:41], v[212:215], v172, v172 op_sel:[0,1,0] op_sel_hi:[0,0,0]
	s_waitcnt lgkmcnt(0)
	v_mfma_scale_f32_16x16x128_f8f6f4 v[78:81], v[2:9], v[42:49], v[216:219], v172, v172 op_sel:[0,1,0] op_sel_hi:[0,0,0]
	v_mfma_scale_f32_16x16x128_f8f6f4 v[74:77], v[18:25], v[42:49], v[220:223], v172, v172 op_sel:[0,1,0] op_sel_hi:[0,0,0]
	s_setprio 0
	s_setprio 1
	v_mfma_scale_f32_16x16x128_f8f6f4 v[118:121], v[130:137], v[10:17], v[118:121], v172, v172 op_sel:[0,1,0] op_sel_hi:[0,0,0]
	v_mfma_scale_f32_16x16x128_f8f6f4 v[114:117], v[138:145], v[10:17], v[114:117], v172, v172 op_sel:[0,1,0] op_sel_hi:[0,0,0]
	v_mfma_scale_f32_16x16x128_f8f6f4 v[102:105], v[130:137], v[26:33], v[102:105], v172, v172 op_sel:[0,1,0] op_sel_hi:[0,0,0]
	v_mfma_scale_f32_16x16x128_f8f6f4 v[98:101], v[138:145], v[26:33], v[98:101], v172, v172 op_sel:[0,1,0] op_sel_hi:[0,0,0]
	v_mfma_scale_f32_16x16x128_f8f6f4 v[86:89], v[130:137], v[34:41], v[176:179], v172, v172 op_sel:[0,1,0] op_sel_hi:[0,0,0]
	v_mfma_scale_f32_16x16x128_f8f6f4 v[82:85], v[138:145], v[34:41], v[180:183], v172, v172 op_sel:[0,1,0] op_sel_hi:[0,0,0]
	v_mfma_scale_f32_16x16x128_f8f6f4 v[70:73], v[130:137], v[42:49], v[184:187], v172, v172 op_sel:[0,1,0] op_sel_hi:[0,0,0]
	v_mfma_scale_f32_16x16x128_f8f6f4 v[66:69], v[138:145], v[42:49], v[188:191], v172, v172 op_sel:[0,1,0] op_sel_hi:[0,0,0]
	s_setprio 0
	s_barrier
; #define PG8_STAGE(bufoff, goff, voff) do { _Pragma("unroll") for (int _i = 0; _i < 2; ++_i) \
;         __builtin_amdgcn_raw_ptr_buffer_load_lds(rsrc, (PG8_LAS void*)(lds + (bufoff) + ldsw + _i * 8192), 16, (int)(voff), (int)((goff) + _i * p1##voff), 0, 0); } while (0)
; #define PG8_LDA(dst, b, h) do { _Pragma("unroll") for (int m = 0; m < 4; ++m) dst[m] = PG8_LD8(lds + PG8_SA(b, h) + aoff + m * 2048); } while (0)
; #define PG8_WAIT_V(n) asm volatile("s_waitcnt vmcnt(" #n ")" ::: "memory")
; #define PG8_WAIT_L(n) asm volatile("s_waitcnt lgkmcnt(" #n ")" ::: "memory")
; #define PG8_BAR __builtin_amdgcn_s_barrier()
; #define PG8_SCHED __builtin_amdgcn_sched_barrier(0)
; template <class Epi, class Sched, bool ALIGN_EPI, bool F8 = false, int F8SC = F8_SCALES>
; __device__ __forceinline__ void gemm_phase(PG8_LAS unsigned char* lds, const __amdgpu_buffer_rsrc_t rsrc, const int lda, const int ldb, const int K, const Sched& S, const Epi& E) {
;     ...
;             PG8_LDA(At, 1, 1); PG8_STAGE(PG8_SB(1, 0), b3, voffB); PG8_STAGE(PG8_SB(1, 1), b3 + hsB, voffB); PG8_STAGE(PG8_SA(1, 0), a3, voffA);
;             PG8_WAIT_V(8); PG8_WAIT_L(0); PG8_BAR; PG8_MMA(1, 0, At, B0); PG8_MMA(1, 1, At, B1); PG8_BAR; PG8_SCHED;
;         }
;         if constexpr (ALIGN_EPI) { if (wr == 0) PG8_BAR; }
	s_mov_b32 m0, s24
	s_add_i32 s53, s52, 0x80
	ds_read_b128 v[34:37], v171 offset:49152
	ds_read_b128 v[38:41], v171 offset:50176
	ds_read_b128 v[150:153], v171 offset:51200
	ds_read_b128 v[154:157], v171 offset:52224
	ds_read_b128 v[158:161], v171 offset:53248
	ds_read_b128 v[162:165], v171 offset:54272
	ds_read_b128 v[176:179], v171 offset:55296
	ds_read_b128 v[180:183], v171 offset:56320
	buffer_load_dwordx4 v168, s[80:83], s53 offen lds
	s_add_i32 s53, s52, 0x20080
	s_mov_b32 m0, s25
	s_add_i32 s50, s50, 0x20080
	buffer_load_dwordx4 v168, s[80:83], s53 offen lds
	s_add_i32 s53, s52, 0x40080
	s_mov_b32 m0, s28
	s_add_i32 s52, s52, 0x60080
	buffer_load_dwordx4 v168, s[80:83], s53 offen lds
	s_mov_b32 m0, s29
	s_nop 0
	buffer_load_dwordx4 v168, s[80:83], s52 offen lds
	s_mov_b32 m0, s26
	s_nop 0
	buffer_load_dwordx4 v1, s[80:83], s51 offen lds
	s_mov_b32 m0, s27
	s_nop 0
	buffer_load_dwordx4 v1, s[80:83], s50 offen lds
	s_waitcnt vmcnt(8)
	s_waitcnt lgkmcnt(0)
	s_barrier
	s_setprio 1
	s_waitcnt lgkmcnt(6)
	v_mfma_scale_f32_16x16x128_f8f6f4 v[62:65], v[2:9], v[34:41], v[62:65], v172, v172 op_sel:[0,1,0] op_sel_hi:[0,0,0]
	v_mfma_scale_f32_16x16x128_f8f6f4 v[58:61], v[18:25], v[34:41], v[58:61], v172, v172 op_sel:[0,1,0] op_sel_hi:[0,0,0]
	s_waitcnt lgkmcnt(4)
	v_mfma_scale_f32_16x16x128_f8f6f4 v[46:49], v[2:9], v[150:157], v[192:195], v172, v172 op_sel:[0,1,0] op_sel_hi:[0,0,0]
	v_mfma_scale_f32_16x16x128_f8f6f4 v[42:45], v[18:25], v[150:157], v[196:199], v172, v172 op_sel:[0,1,0] op_sel_hi:[0,0,0]
	s_waitcnt lgkmcnt(2)
	v_mfma_scale_f32_16x16x128_f8f6f4 v[30:33], v[2:9], v[158:165], v[200:203], v172, v172 op_sel:[0,1,0] op_sel_hi:[0,0,0]
	v_mfma_scale_f32_16x16x128_f8f6f4 v[26:29], v[18:25], v[158:165], v[204:207], v172, v172 op_sel:[0,1,0] op_sel_hi:[0,0,0]
	s_waitcnt lgkmcnt(0)
	v_mfma_scale_f32_16x16x128_f8f6f4 v[14:17], v[2:9], v[176:183], v[224:227], v172, v172 op_sel:[0,1,0] op_sel_hi:[0,0,0]
	v_mfma_scale_f32_16x16x128_f8f6f4 v[10:13], v[18:25], v[176:183], v[228:231], v172, v172 op_sel:[0,1,0] op_sel_hi:[0,0,0]
	s_setprio 0
	s_setprio 1
	v_mfma_scale_f32_16x16x128_f8f6f4 v[54:57], v[130:137], v[34:41], v[54:57], v172, v172 op_sel:[0,1,0] op_sel_hi:[0,0,0]
	v_mfma_scale_f32_16x16x128_f8f6f4 v[50:53], v[138:145], v[34:41], v[50:53], v172, v172 op_sel:[0,1,0] op_sel_hi:[0,0,0]
	v_mfma_scale_f32_16x16x128_f8f6f4 v[38:41], v[130:137], v[150:157], v[232:235], v172, v172 op_sel:[0,1,0] op_sel_hi:[0,0,0]
	v_mfma_scale_f32_16x16x128_f8f6f4 v[34:37], v[138:145], v[150:157], v[236:239], v172, v172 op_sel:[0,1,0] op_sel_hi:[0,0,0]
	v_mfma_scale_f32_16x16x128_f8f6f4 v[22:25], v[130:137], v[158:165], v[240:243], v172, v172 op_sel:[0,1,0] op_sel_hi:[0,0,0]
	v_mfma_scale_f32_16x16x128_f8f6f4 v[18:21], v[138:145], v[158:165], v[244:247], v172, v172 op_sel:[0,1,0] op_sel_hi:[0,0,0]
	v_mfma_scale_f32_16x16x128_f8f6f4 v[6:9], v[130:137], v[176:183], v[248:251], v172, v172 op_sel:[0,1,0] op_sel_hi:[0,0,0]
	v_mfma_scale_f32_16x16x128_f8f6f4 v[2:5], v[138:145], v[176:183], v[146:149], v172, v172 op_sel:[0,1,0] op_sel_hi:[0,0,0]
	s_setprio 0
	s_barrier
	s_add_i32 s49, s49, 2
	s_addk_i32 s4, 0x100
	s_addk_i32 s5, 0x100
	s_cmp_gt_u32 s49, 13
	s_cbranch_scc0 .LBB0_1725
	s_and_b64 vcc, exec, s[10:11]
	s_cbranch_vccz .LBB0_1728
	s_barrier
; #define EPI_ROWLOOP _Pragma("unroll") for (int ai = 0; ai < 2; ++ai) _Pragma("unroll") for (int m = 0; m < 4; ++m)
;     __device__ __forceinline__ bool operator()(f32x4 (&acc)[2][2][4][2], const Unit& u, int wr, int wc, int fr, int fq) const {
;         const int row0 = u.pm * BM + wr * 64 + fr, col0 = u.pn * BM + wc * 32 + 8 * fq;
;         const float* bp = bdn + (size_t)u.aux * D + col0;
;         f32x4 bv[2][2];
; #pragma unroll
;         for (int bj = 0; bj < 2; ++bj)
; #pragma unroll
;             for (int n = 0; n < 2; ++n) bv[bj][n] = *(const f32x4*)(bp + bj * HALF + 4 * n);
;         int slots[8]; float ws_[8];
; #pragma unroll
;         for (int q = 0; q < 8; ++q) { const int row = row0 + (q >> 2) * HALF + (q & 3) * 16; slots[q] = rowslot[row]; ws_[q] = roww[row]; }
;         EPI_ROWLOOP { const int slot = slots[ai * 4 + m]; const float w = ws_[ai * 4 + m] * YS_SCALE;
;             if (slot >= 0) { unsigned char* rowp = YS + (size_t)slot * D + col0;
; #pragma unroll
;                 for (int bj = 0; bj < 2; ++bj) { const f32x4 o0 = (acc[ai][bj][m][0] + bv[bj][0]) * w, o1 = (acc[ai][bj][m][1] + bv[bj][1]) * w;
.LBB0_1728:
	v_mov_b32_e32 v146, v0
	s_lshl_b32 s4, s13, 8
	v_readfirstlane_b32 s49, v146
	s_lshr_b32 s5, s49, 1
	s_and_b32 s5, s5, 0x60
	s_or_b32 s4, s5, s4
	v_lshrrev_b32_e32 v130, 1, v146
	s_ashr_i32 s13, s12, 31
	v_and_or_b32 v150, v130, 24, s4
	s_lshl_b64 s[4:5], s[12:13], 13
	s_add_u32 s4, s72, s4
	s_addc_u32 s5, s73, s5
	v_ashrrev_i32_e32 v151, 31, v150
	v_lshl_add_u64 v[134:135], v[150:151], 2, s[4:5]
	s_ashr_i32 s4, s49, 2
	s_andn2_b32 s4, s4, 63
	v_and_or_b32 v146, v146, 15, s4
	v_lshl_add_u32 v166, s48, 8, v146
	v_or_b32_e32 v152, 16, v166
	v_or_b32_e32 v156, 32, v166
	v_ashrrev_i32_e32 v167, 31, v166
	v_ashrrev_i32_e32 v153, 31, v152
	v_ashrrev_i32_e32 v157, 31, v156
	v_or_b32_e32 v160, 48, v166
	v_lshlrev_b64 v[146:147], 2, v[166:167]
	v_lshlrev_b64 v[152:153], 2, v[152:153]
	v_lshlrev_b64 v[156:157], 2, v[156:157]
	v_ashrrev_i32_e32 v161, 31, v160
	v_lshl_add_u64 v[148:149], s[6:7], 0, v[146:147]
	v_lshl_add_u64 v[154:155], s[6:7], 0, v[152:153]
	v_lshl_add_u64 v[158:159], s[6:7], 0, v[156:157]
	v_lshlrev_b64 v[160:161], 2, v[160:161]
	global_load_dwordx4 v[138:141], v[134:135], off offset:16
	global_load_dwordx4 v[142:145], v[134:135], off
	global_load_dwordx4 v[130:133], v[134:135], off offset:528
	s_nop 0
	global_load_dwordx4 v[134:137], v[134:135], off offset:512
	v_lshl_add_u64 v[152:153], s[8:9], 0, v[152:153]
	v_lshl_add_u64 v[156:157], s[8:9], 0, v[156:157]
	v_lshl_add_u64 v[176:177], s[6:7], 0, v[160:161]
	v_lshl_add_u64 v[178:179], s[8:9], 0, v[160:161]
	global_load_dword v184, v[148:149], off
	global_load_dword v164, v[154:155], off
	global_load_dword v165, v[152:153], off
	global_load_dword v162, v[158:159], off
	global_load_dword v163, v[156:157], off
	global_load_dword v160, v[176:177], off
	global_load_dword v161, v[178:179], off
	s_nop 0
	global_load_dword v158, v[148:149], off offset:512
	v_add_u32_e32 v154, 0xa0, v166
	v_ashrrev_i32_e32 v155, 31, v154
	v_add_u32_e32 v148, 0x90, v166
	v_lshlrev_b64 v[154:155], 2, v[154:155]
	v_ashrrev_i32_e32 v149, 31, v148
	v_lshl_add_u64 v[176:177], s[6:7], 0, v[154:155]
	v_lshl_add_u64 v[178:179], s[8:9], 0, v[154:155]
	v_add_u32_e32 v154, 0xb0, v166
	v_lshlrev_b64 v[148:149], 2, v[148:149]
	v_ashrrev_i32_e32 v155, 31, v154
	v_lshl_add_u64 v[146:147], s[8:9], 0, v[146:147]
	v_lshl_add_u64 v[152:153], s[6:7], 0, v[148:149]
	v_lshlrev_b64 v[154:155], 2, v[154:155]
	v_lshl_add_u64 v[148:149], s[8:9], 0, v[148:149]
	v_lshl_add_u64 v[180:181], s[6:7], 0, v[154:155]
	v_lshl_add_u64 v[182:183], s[8:9], 0, v[154:155]
	global_load_dword v159, v[146:147], off offset:512
	global_load_dword v156, v[152:153], off
	global_load_dword v157, v[148:149], off
	global_load_dword v154, v[176:177], off
	global_load_dword v155, v[178:179], off
	s_nop 0
	global_load_dword v152, v[180:181], off
	global_load_dword v153, v[182:183], off
	v_mov_b32_e32 v185, v175
	s_waitcnt vmcnt(0)
	v_cmp_lt_i32_e32 vcc, -1, v184
	s_and_saveexec_b64 s[4:5], vcc
	s_cbranch_execz .LBB0_1737
	v_lshl_add_u64 v[146:147], v[166:167], 2, s[8:9]
	global_load_dword v175, v[146:147], off
	v_pk_add_f32 v[126:127], v[126:127], v[142:143]
	v_pk_add_f32 v[122:123], v[122:123], v[138:139]
	v_mov_b32_e32 v148, v185
	v_mov_b32_e32 v149, v185
	v_pk_add_f32 v[118:119], v[118:119], v[134:135]
	v_pk_add_f32 v[114:115], v[114:115], v[130:131]
	v_mov_b32_e32 v166, v185
	v_mov_b32_e32 v167, v185
	v_pk_add_f32 v[128:129], v[128:129], v[144:145]
	v_pk_add_f32 v[124:125], v[124:125], v[140:141]
	v_pk_add_f32 v[120:121], v[120:121], v[136:137]
	v_pk_add_f32 v[116:117], v[116:117], v[132:133]
	v_lshlrev_b64 v[146:147], 11, v[184:185]
	s_waitcnt vmcnt(0)
	v_mul_f32_e32 v176, 0x41800000, v175
	v_pk_mul_f32 v[126:127], v[126:127], v[176:177] op_sel_hi:[1,0]
	v_pk_mul_f32 v[122:123], v[122:123], v[176:177] op_sel_hi:[1,0]
	v_pk_mul_f32 v[118:119], v[118:119], v[176:177] op_sel_hi:[1,0]
	v_pk_mul_f32 v[114:115], v[114:115], v[176:177] op_sel_hi:[1,0]
	v_cvt_pk_fp8_f32 v148, v126, v127
	v_cvt_pk_fp8_f32 v149, v122, v123
	v_cvt_pk_fp8_f32 v166, v118, v119
	v_cvt_pk_fp8_f32 v167, v114, v115
	v_pk_mul_f32 v[128:129], v[128:129], v[176:177] op_sel_hi:[1,0]
	v_pk_mul_f32 v[124:125], v[124:125], v[176:177] op_sel_hi:[1,0]
	v_pk_mul_f32 v[120:121], v[120:121], v[176:177] op_sel_hi:[1,0]
	v_pk_mul_f32 v[116:117], v[116:117], v[176:177] op_sel_hi:[1,0]
	v_cvt_pk_fp8_f32 v148, v128, v129 op_sel:[0,0,1]
	v_cvt_pk_fp8_f32 v149, v124, v125 op_sel:[0,0,1]
	v_cvt_pk_fp8_f32 v166, v120, v121 op_sel:[0,0,1]
	v_cvt_pk_fp8_f32 v167, v116, v117 op_sel:[0,0,1]
	v_lshl_add_u64 v[114:115], s[88:89], 0, v[146:147]
	v_lshl_add_u64 v[114:115], v[114:115], 0, v[150:151]
	global_store_dwordx2 v[114:115], v[148:149], off
	global_store_dwordx2 v[114:115], v[166:167], off offset:128
	s_or_b64 exec, exec, s[4:5]
	v_cmp_lt_i32_e32 vcc, -1, v164
	s_and_saveexec_b64 s[4:5], vcc
	s_cbranch_execnz .LBB0_1738
